# PEER u-sweep: workgroup barrier every second column slice (was every slice) + hoisted gather offsets
# speedup vs baseline: 1.0570x; 1.0038x over previous
; #define LAS __attribute__((address_space(3)))
; __device__ __forceinline__ void peer_expert_phase(const Args& a, int layer, LAS unsigned char* lds, int G, int bid) {
;     ...
;         for (int sidx = 0; sidx < 32; ++sidx) { const int s = (sidx + srot) & 31; const unsigned char* pus = PU + s * 128;
; #pragma unroll
;             for (int i = 0; i < 4; ++i) {
;                 int tok = tb + i * NGW; tok = tok < NTOK ? tok : tb;
;                 const u32x4 xq = *(const LAS u32x4*)(X8 + i * 4096 + s * 128 + 16 * l7);
;                 u32x4 r[16];
; #pragma unroll
;                 for (int c = 0; c < 16; ++c) { const unsigned eo = (unsigned)__shfl((int)(c < 8 ? eoa[i] : eob[i]), (8 * c + g8) & 63); r[c] = *(const u32x4*)(pus + (eo + lo16)); }
; #pragma unroll
;                 for (int c = 0; c < 16; ++c) { int d = pacc[i][c];
; #pragma unroll
;                     for (int q = 0; q < 4; ++q) d = __builtin_amdgcn_sdot4((int)r[c][q], (int)xq[q], d, false);
;                     pacc[i][c] = d; }
;                 __builtin_amdgcn_sched_barrier(0);
.LBB0_1206:
	s_bitcmp0_b32 s50, 7
	s_cbranch_scc0 .Lubar0_skip
	s_barrier
.Lubar0_skip:
	s_add_i32 s34, s80, s50
	s_and_b32 s34, s34, 0xf80
	s_add_u32 s70, s33, s34
	s_addc_u32 s71, s72, 0
	v_add_u32_e32 v121, s34, v43
	global_load_dwordx4 v[122:125], v190, s[70:71]
	global_load_dwordx4 v[126:129], v191, s[70:71]
	global_load_dwordx4 v[130:133], v192, s[70:71]
	global_load_dwordx4 v[134:137], v193, s[70:71]
	global_load_dwordx4 v[138:141], v194, s[70:71]
	global_load_dwordx4 v[142:145], v195, s[70:71]
	global_load_dwordx4 v[146:149], v196, s[70:71]
	global_load_dwordx4 v[150:153], v197, s[70:71]
	global_load_dwordx4 v[154:157], v198, s[70:71]
	global_load_dwordx4 v[162:165], v199, s[70:71]
	global_load_dwordx4 v[170:173], v200, s[70:71]
	global_load_dwordx4 v[158:161], v201, s[70:71]
	global_load_dwordx4 v[178:181], v202, s[70:71]
	global_load_dwordx4 v[166:169], v203, s[70:71]
	global_load_dwordx4 v[174:177], v204, s[70:71]
	global_load_dwordx4 v[182:185], v205, s[70:71]
	ds_read_b128 v[186:189], v121
	s_waitcnt lgkmcnt(0)
	s_waitcnt vmcnt(15)
	v_dot4c_i32_i8_e32 v120, v122, v186
	s_waitcnt vmcnt(14)
	v_dot4c_i32_i8_e32 v119, v126, v186
	v_dot4c_i32_i8_e32 v120, v123, v187
	s_waitcnt vmcnt(13)
	v_dot4c_i32_i8_e32 v33, v130, v186
	s_waitcnt vmcnt(12)
	v_dot4c_i32_i8_e32 v118, v134, v186
	v_dot4c_i32_i8_e32 v119, v127, v187
	v_dot4c_i32_i8_e32 v33, v131, v187
	v_dot4c_i32_i8_e32 v118, v135, v187
	s_waitcnt vmcnt(11)
	v_dot4c_i32_i8_e32 v117, v138, v186
	s_waitcnt vmcnt(10)
	v_dot4c_i32_i8_e32 v116, v142, v186
	v_dot4c_i32_i8_e32 v117, v139, v187
	v_dot4c_i32_i8_e32 v116, v143, v187
	v_dot4c_i32_i8_e32 v120, v124, v188
	s_waitcnt vmcnt(9)
	v_dot4c_i32_i8_e32 v115, v146, v186
	s_waitcnt vmcnt(8)
	v_dot4c_i32_i8_e32 v114, v150, v186
	v_dot4c_i32_i8_e32 v115, v147, v187
	v_dot4c_i32_i8_e32 v114, v151, v187
	s_waitcnt vmcnt(7)
	v_dot4c_i32_i8_e32 v113, v154, v186
	v_dot4c_i32_i8_e32 v113, v155, v187
	s_waitcnt vmcnt(6)
	v_dot4c_i32_i8_e32 v32, v162, v186
	v_dot4c_i32_i8_e32 v32, v163, v187
	v_dot4c_i32_i8_e32 v119, v128, v188
	v_dot4c_i32_i8_e32 v33, v132, v188
	v_dot4c_i32_i8_e32 v118, v136, v188
	s_waitcnt vmcnt(5)
	v_dot4c_i32_i8_e32 v110, v170, v186
	v_dot4c_i32_i8_e32 v110, v171, v187
	s_waitcnt vmcnt(4)
	v_dot4c_i32_i8_e32 v112, v158, v186
	v_dot4c_i32_i8_e32 v112, v159, v187
	v_dot4c_i32_i8_e32 v117, v140, v188
	s_waitcnt vmcnt(3)
	v_dot4c_i32_i8_e32 v108, v178, v186
	v_dot4c_i32_i8_e32 v108, v179, v187
	v_dot4c_i32_i8_e32 v116, v144, v188
	v_dot4c_i32_i8_e32 v115, v148, v188
	s_waitcnt vmcnt(2)
	v_dot4c_i32_i8_e32 v111, v166, v186
	v_dot4c_i32_i8_e32 v111, v167, v187
	v_dot4c_i32_i8_e32 v114, v152, v188
	v_dot4c_i32_i8_e32 v113, v156, v188
	v_dot4c_i32_i8_e32 v112, v160, v188
	v_dot4c_i32_i8_e32 v32, v164, v188
	v_dot4c_i32_i8_e32 v111, v168, v188
	s_waitcnt vmcnt(1)
	v_dot4c_i32_i8_e32 v109, v174, v186
	v_dot4c_i32_i8_e32 v109, v175, v187
	v_dot4c_i32_i8_e32 v110, v172, v188
	v_dot4c_i32_i8_e32 v109, v176, v188
	v_dot4c_i32_i8_e32 v108, v180, v188
	v_dot4c_i32_i8_e32 v120, v125, v189
	v_dot4c_i32_i8_e32 v119, v129, v189
	s_waitcnt vmcnt(0)
	v_dot4c_i32_i8_e32 v107, v182, v186
	v_dot4c_i32_i8_e32 v107, v183, v187
	v_dot4c_i32_i8_e32 v107, v184, v188
	v_dot4c_i32_i8_e32 v33, v133, v189
	v_dot4c_i32_i8_e32 v118, v137, v189
	v_dot4c_i32_i8_e32 v117, v141, v189
	v_dot4c_i32_i8_e32 v116, v145, v189
	v_dot4c_i32_i8_e32 v115, v149, v189
	v_dot4c_i32_i8_e32 v114, v153, v189
	v_dot4c_i32_i8_e32 v113, v157, v189
	v_dot4c_i32_i8_e32 v112, v161, v189
	v_dot4c_i32_i8_e32 v32, v165, v189
	v_dot4c_i32_i8_e32 v111, v169, v189
	v_dot4c_i32_i8_e32 v110, v173, v189
	v_dot4c_i32_i8_e32 v109, v177, v189
	v_dot4c_i32_i8_e32 v108, v181, v189
	v_dot4c_i32_i8_e32 v107, v185, v189
	global_load_dwordx4 v[122:125], v206, s[70:71]
	global_load_dwordx4 v[126:129], v207, s[70:71]
	global_load_dwordx4 v[130:133], v208, s[70:71]
	global_load_dwordx4 v[134:137], v209, s[70:71]
	global_load_dwordx4 v[138:141], v210, s[70:71]
	global_load_dwordx4 v[142:145], v211, s[70:71]
	global_load_dwordx4 v[146:149], v212, s[70:71]
	global_load_dwordx4 v[150:153], v213, s[70:71]
	global_load_dwordx4 v[154:157], v214, s[70:71]
	global_load_dwordx4 v[158:161], v215, s[70:71]
	global_load_dwordx4 v[162:165], v216, s[70:71]
	global_load_dwordx4 v[166:169], v217, s[70:71]
	global_load_dwordx4 v[170:173], v218, s[70:71]
	global_load_dwordx4 v[174:177], v219, s[70:71]
	global_load_dwordx4 v[178:181], v220, s[70:71]
	global_load_dwordx4 v[182:185], v221, s[70:71]
	ds_read_b128 v[186:189], v121 offset:4096
	s_waitcnt lgkmcnt(0)
	s_waitcnt vmcnt(15)
	v_dot4c_i32_i8_e32 v106, v122, v186
	s_waitcnt vmcnt(14)
	v_dot4c_i32_i8_e32 v105, v126, v186
	s_waitcnt vmcnt(13)
	v_dot4c_i32_i8_e32 v104, v130, v186
	s_waitcnt vmcnt(12)
	v_dot4c_i32_i8_e32 v103, v134, v186
	s_waitcnt vmcnt(11)
	v_dot4c_i32_i8_e32 v102, v138, v186
	s_waitcnt vmcnt(10)
	v_dot4c_i32_i8_e32 v101, v142, v186
	s_waitcnt vmcnt(9)
	v_dot4c_i32_i8_e32 v100, v146, v186
	s_waitcnt vmcnt(8)
	v_dot4c_i32_i8_e32 v99, v150, v186
	s_waitcnt vmcnt(7)
	v_dot4c_i32_i8_e32 v98, v154, v186
	s_waitcnt vmcnt(6)
	v_dot4c_i32_i8_e32 v97, v158, v186
	s_waitcnt vmcnt(5)
; #define LAS __attribute__((address_space(3)))
; __device__ __forceinline__ void peer_expert_phase(const Args& a, int layer, LAS unsigned char* lds, int G, int bid) {
;     ...
;             for (int i = 0; i < 4; ++i) {
;                 int tok = tb + i * NGW; tok = tok < NTOK ? tok : tb;
;                 const u32x4 xq = *(const LAS u32x4*)(X8 + i * 4096 + s * 128 + 16 * l7);
;                 u32x4 r[16];
; #pragma unroll
;                 for (int c = 0; c < 16; ++c) { const unsigned eo = (unsigned)__shfl((int)(c < 8 ? eoa[i] : eob[i]), (8 * c + g8) & 63); r[c] = *(const u32x4*)(pus + (eo + lo16)); }
; #pragma unroll
;                 for (int c = 0; c < 16; ++c) { int d = pacc[i][c];
; #pragma unroll
;                     for (int q = 0; q < 4; ++q) d = __builtin_amdgcn_sdot4((int)r[c][q], (int)xq[q], d, false);
;                     pacc[i][c] = d; }
;                 __builtin_amdgcn_sched_barrier(0);
	v_dot4c_i32_i8_e32 v96, v162, v186
	v_dot4c_i32_i8_e32 v106, v123, v187
	v_dot4c_i32_i8_e32 v105, v127, v187
	v_dot4c_i32_i8_e32 v104, v131, v187
	v_dot4c_i32_i8_e32 v103, v135, v187
	v_dot4c_i32_i8_e32 v102, v139, v187
	v_dot4c_i32_i8_e32 v101, v143, v187
	v_dot4c_i32_i8_e32 v100, v147, v187
	v_dot4c_i32_i8_e32 v99, v151, v187
	v_dot4c_i32_i8_e32 v98, v155, v187
	v_dot4c_i32_i8_e32 v97, v159, v187
	v_dot4c_i32_i8_e32 v96, v163, v187
	v_dot4c_i32_i8_e32 v106, v124, v188
	v_dot4c_i32_i8_e32 v105, v128, v188
	v_dot4c_i32_i8_e32 v104, v132, v188
	v_dot4c_i32_i8_e32 v103, v136, v188
	v_dot4c_i32_i8_e32 v102, v140, v188
	v_dot4c_i32_i8_e32 v101, v144, v188
	v_dot4c_i32_i8_e32 v100, v148, v188
	v_dot4c_i32_i8_e32 v99, v152, v188
	v_dot4c_i32_i8_e32 v98, v156, v188
	v_dot4c_i32_i8_e32 v97, v160, v188
	v_dot4c_i32_i8_e32 v96, v164, v188
	v_dot4c_i32_i8_e32 v106, v125, v189
	v_dot4c_i32_i8_e32 v105, v129, v189
	v_dot4c_i32_i8_e32 v104, v133, v189
	v_dot4c_i32_i8_e32 v103, v137, v189
	v_dot4c_i32_i8_e32 v102, v141, v189
	v_dot4c_i32_i8_e32 v101, v145, v189
	v_dot4c_i32_i8_e32 v100, v149, v189
	v_dot4c_i32_i8_e32 v99, v153, v189
	v_dot4c_i32_i8_e32 v98, v157, v189
	v_dot4c_i32_i8_e32 v97, v161, v189
	v_dot4c_i32_i8_e32 v96, v165, v189
	s_waitcnt vmcnt(4)
	v_dot4c_i32_i8_e32 v93, v166, v186
	v_dot4c_i32_i8_e32 v93, v167, v187
	s_waitcnt vmcnt(3)
	v_dot4c_i32_i8_e32 v95, v170, v186
	v_dot4c_i32_i8_e32 v95, v171, v187
	s_waitcnt vmcnt(2)
	v_dot4c_i32_i8_e32 v94, v174, v186
	v_dot4c_i32_i8_e32 v94, v175, v187
	s_waitcnt vmcnt(1)
	v_dot4c_i32_i8_e32 v92, v178, v186
	v_dot4c_i32_i8_e32 v92, v179, v187
	s_waitcnt vmcnt(0)
	v_dot4c_i32_i8_e32 v91, v182, v186
	v_dot4c_i32_i8_e32 v91, v183, v187
	v_dot4c_i32_i8_e32 v93, v168, v188
	v_dot4c_i32_i8_e32 v95, v172, v188
	v_dot4c_i32_i8_e32 v94, v176, v188
	v_dot4c_i32_i8_e32 v92, v180, v188
	v_dot4c_i32_i8_e32 v91, v184, v188
	v_dot4c_i32_i8_e32 v93, v169, v189
	v_dot4c_i32_i8_e32 v95, v173, v189
	v_dot4c_i32_i8_e32 v94, v177, v189
	v_dot4c_i32_i8_e32 v92, v181, v189
	v_dot4c_i32_i8_e32 v91, v185, v189
	global_load_dwordx4 v[122:125], v222, s[70:71]
	global_load_dwordx4 v[126:129], v223, s[70:71]
	global_load_dwordx4 v[130:133], v224, s[70:71]
	global_load_dwordx4 v[134:137], v225, s[70:71]
	global_load_dwordx4 v[138:141], v226, s[70:71]
	global_load_dwordx4 v[142:145], v227, s[70:71]
	global_load_dwordx4 v[146:149], v229, s[70:71]
	global_load_dwordx4 v[150:153], v230, s[70:71]
	global_load_dwordx4 v[154:157], v231, s[70:71]
	global_load_dwordx4 v[158:161], v232, s[70:71]
	global_load_dwordx4 v[162:165], v233, s[70:71]
	global_load_dwordx4 v[166:169], v234, s[70:71]
	global_load_dwordx4 v[170:173], v235, s[70:71]
	global_load_dwordx4 v[174:177], v236, s[70:71]
	global_load_dwordx4 v[178:181], v237, s[70:71]
	global_load_dwordx4 v[182:185], v238, s[70:71]
	ds_read_b128 v[186:189], v121 offset:8192
	s_waitcnt lgkmcnt(0)
	s_waitcnt vmcnt(15)
	v_dot4c_i32_i8_e32 v90, v122, v186
	s_waitcnt vmcnt(14)
	v_dot4c_i32_i8_e32 v89, v126, v186
	s_waitcnt vmcnt(13)
	v_dot4c_i32_i8_e32 v88, v130, v186
	s_waitcnt vmcnt(12)
	v_dot4c_i32_i8_e32 v87, v134, v186
	s_waitcnt vmcnt(11)
	v_dot4c_i32_i8_e32 v86, v138, v186
	s_waitcnt vmcnt(10)
	v_dot4c_i32_i8_e32 v85, v142, v186
	s_waitcnt vmcnt(9)
	v_dot4c_i32_i8_e32 v84, v146, v186
	s_waitcnt vmcnt(8)
	v_dot4c_i32_i8_e32 v83, v150, v186
	s_waitcnt vmcnt(7)
	v_dot4c_i32_i8_e32 v82, v154, v186
	s_waitcnt vmcnt(6)
	v_dot4c_i32_i8_e32 v81, v158, v186
	s_waitcnt vmcnt(5)
	v_dot4c_i32_i8_e32 v80, v162, v186
	v_dot4c_i32_i8_e32 v90, v123, v187
	v_dot4c_i32_i8_e32 v89, v127, v187
	v_dot4c_i32_i8_e32 v88, v131, v187
	v_dot4c_i32_i8_e32 v87, v135, v187
	v_dot4c_i32_i8_e32 v86, v139, v187
	v_dot4c_i32_i8_e32 v85, v143, v187
	v_dot4c_i32_i8_e32 v84, v147, v187
	v_dot4c_i32_i8_e32 v83, v151, v187
	v_dot4c_i32_i8_e32 v82, v155, v187
	v_dot4c_i32_i8_e32 v81, v159, v187
	v_dot4c_i32_i8_e32 v80, v163, v187
	v_dot4c_i32_i8_e32 v90, v124, v188
	v_dot4c_i32_i8_e32 v89, v128, v188
	v_dot4c_i32_i8_e32 v88, v132, v188
	v_dot4c_i32_i8_e32 v87, v136, v188
	v_dot4c_i32_i8_e32 v86, v140, v188
	v_dot4c_i32_i8_e32 v85, v144, v188
	v_dot4c_i32_i8_e32 v84, v148, v188
	v_dot4c_i32_i8_e32 v83, v152, v188
	v_dot4c_i32_i8_e32 v82, v156, v188
	v_dot4c_i32_i8_e32 v81, v160, v188
	v_dot4c_i32_i8_e32 v80, v164, v188
	v_dot4c_i32_i8_e32 v90, v125, v189
	v_dot4c_i32_i8_e32 v89, v129, v189
	v_dot4c_i32_i8_e32 v88, v133, v189
	v_dot4c_i32_i8_e32 v87, v137, v189
	v_dot4c_i32_i8_e32 v86, v141, v189
	v_dot4c_i32_i8_e32 v85, v145, v189
	v_dot4c_i32_i8_e32 v84, v149, v189
	v_dot4c_i32_i8_e32 v83, v153, v189
	v_dot4c_i32_i8_e32 v82, v157, v189
	v_dot4c_i32_i8_e32 v81, v161, v189
	v_dot4c_i32_i8_e32 v80, v165, v189
	s_waitcnt vmcnt(4)
	v_dot4c_i32_i8_e32 v79, v166, v186
	v_dot4c_i32_i8_e32 v79, v167, v187
	s_waitcnt vmcnt(3)
	v_dot4c_i32_i8_e32 v78, v170, v186
	v_dot4c_i32_i8_e32 v78, v171, v187
	s_waitcnt vmcnt(2)
	v_dot4c_i32_i8_e32 v77, v174, v186
	v_dot4c_i32_i8_e32 v77, v175, v187
	s_waitcnt vmcnt(1)
	v_dot4c_i32_i8_e32 v76, v178, v186
	v_dot4c_i32_i8_e32 v76, v179, v187
	s_waitcnt vmcnt(0)
; #define LAS __attribute__((address_space(3)))
; __device__ __forceinline__ void peer_expert_phase(const Args& a, int layer, LAS unsigned char* lds, int G, int bid) {
;     ...
;             for (int i = 0; i < 4; ++i) {
;                 int tok = tb + i * NGW; tok = tok < NTOK ? tok : tb;
;                 const u32x4 xq = *(const LAS u32x4*)(X8 + i * 4096 + s * 128 + 16 * l7);
;                 u32x4 r[16];
; #pragma unroll
;                 for (int c = 0; c < 16; ++c) { const unsigned eo = (unsigned)__shfl((int)(c < 8 ? eoa[i] : eob[i]), (8 * c + g8) & 63); r[c] = *(const u32x4*)(pus + (eo + lo16)); }
; #pragma unroll
;                 for (int c = 0; c < 16; ++c) { int d = pacc[i][c];
; #pragma unroll
;                     for (int q = 0; q < 4; ++q) d = __builtin_amdgcn_sdot4((int)r[c][q], (int)xq[q], d, false);
;                     pacc[i][c] = d; }
;                 __builtin_amdgcn_sched_barrier(0);
;             }
;         }
;         float pa[4], pb[4];
; #pragma unroll
;         for (int i = 0; i < 4; ++i) { pa[i] = 0.f; pb[i] = 0.f;
; #pragma unroll
;             for (int c = 0; c < 16; ++c) { float v = (float)pacc[i][c]; v += __shfl_xor(v, 1); v += __shfl_xor(v, 2); v += __shfl_xor(v, 4);
;                 const float t = __shfl(v, 8 * (lane & 7));
;                 if (c < 8) pa[i] = (g8 == c) ? t : pa[i]; else pb[i] = (g8 == c - 8) ? t : pb[i]; } }
	v_dot4c_i32_i8_e32 v75, v182, v186
	v_dot4c_i32_i8_e32 v75, v183, v187
	v_dot4c_i32_i8_e32 v79, v168, v188
	v_dot4c_i32_i8_e32 v78, v172, v188
	v_dot4c_i32_i8_e32 v77, v176, v188
	v_dot4c_i32_i8_e32 v76, v180, v188
	v_dot4c_i32_i8_e32 v75, v184, v188
	v_dot4c_i32_i8_e32 v79, v169, v189
	v_dot4c_i32_i8_e32 v78, v173, v189
	v_dot4c_i32_i8_e32 v77, v177, v189
	v_dot4c_i32_i8_e32 v76, v181, v189
	v_dot4c_i32_i8_e32 v75, v185, v189
	global_load_dwordx4 v[122:125], v239, s[70:71]
	global_load_dwordx4 v[126:129], v240, s[70:71]
	global_load_dwordx4 v[130:133], v241, s[70:71]
	global_load_dwordx4 v[134:137], v242, s[70:71]
	global_load_dwordx4 v[138:141], v243, s[70:71]
	global_load_dwordx4 v[142:145], v244, s[70:71]
	global_load_dwordx4 v[146:149], v245, s[70:71]
	global_load_dwordx4 v[150:153], v246, s[70:71]
	global_load_dwordx4 v[154:157], v247, s[70:71]
	global_load_dwordx4 v[158:161], v248, s[70:71]
	global_load_dwordx4 v[162:165], v249, s[70:71]
	global_load_dwordx4 v[166:169], v250, s[70:71]
	global_load_dwordx4 v[170:173], v251, s[70:71]
	global_load_dwordx4 v[174:177], v252, s[70:71]
	global_load_dwordx4 v[178:181], v253, s[70:71]
	global_load_dwordx4 v[182:185], v254, s[70:71]
	ds_read_b128 v[186:189], v121 offset:12288
	s_waitcnt lgkmcnt(0)
	s_waitcnt vmcnt(15)
	v_dot4c_i32_i8_e32 v74, v122, v186
	s_waitcnt vmcnt(14)
	v_dot4c_i32_i8_e32 v73, v126, v186
	s_waitcnt vmcnt(13)
	v_dot4c_i32_i8_e32 v72, v130, v186
	s_waitcnt vmcnt(12)
	v_dot4c_i32_i8_e32 v71, v134, v186
	s_waitcnt vmcnt(11)
	v_dot4c_i32_i8_e32 v70, v138, v186
	s_waitcnt vmcnt(10)
	v_dot4c_i32_i8_e32 v69, v142, v186
	s_waitcnt vmcnt(9)
	v_dot4c_i32_i8_e32 v68, v146, v186
	s_waitcnt vmcnt(8)
	v_dot4c_i32_i8_e32 v67, v150, v186
	s_waitcnt vmcnt(7)
	v_dot4c_i32_i8_e32 v66, v154, v186
	s_waitcnt vmcnt(6)
	v_dot4c_i32_i8_e32 v65, v158, v186
	s_waitcnt vmcnt(5)
	v_dot4c_i32_i8_e32 v35, v162, v186
	v_dot4c_i32_i8_e32 v74, v123, v187
	v_dot4c_i32_i8_e32 v73, v127, v187
	v_dot4c_i32_i8_e32 v72, v131, v187
	v_dot4c_i32_i8_e32 v71, v135, v187
	v_dot4c_i32_i8_e32 v70, v139, v187
	v_dot4c_i32_i8_e32 v69, v143, v187
	v_dot4c_i32_i8_e32 v68, v147, v187
	v_dot4c_i32_i8_e32 v67, v151, v187
	v_dot4c_i32_i8_e32 v66, v155, v187
	v_dot4c_i32_i8_e32 v65, v159, v187
	v_dot4c_i32_i8_e32 v35, v163, v187
	v_dot4c_i32_i8_e32 v74, v124, v188
	v_dot4c_i32_i8_e32 v73, v128, v188
	v_dot4c_i32_i8_e32 v72, v132, v188
	v_dot4c_i32_i8_e32 v71, v136, v188
	v_dot4c_i32_i8_e32 v70, v140, v188
	v_dot4c_i32_i8_e32 v69, v144, v188
	v_dot4c_i32_i8_e32 v68, v148, v188
	v_dot4c_i32_i8_e32 v67, v152, v188
	v_dot4c_i32_i8_e32 v66, v156, v188
	v_dot4c_i32_i8_e32 v65, v160, v188
	v_dot4c_i32_i8_e32 v35, v164, v188
	v_dot4c_i32_i8_e32 v74, v125, v189
	v_dot4c_i32_i8_e32 v73, v129, v189
	v_dot4c_i32_i8_e32 v72, v133, v189
	v_dot4c_i32_i8_e32 v71, v137, v189
	v_dot4c_i32_i8_e32 v70, v141, v189
	v_dot4c_i32_i8_e32 v69, v145, v189
	v_dot4c_i32_i8_e32 v68, v149, v189
	v_dot4c_i32_i8_e32 v67, v153, v189
	v_dot4c_i32_i8_e32 v66, v157, v189
	v_dot4c_i32_i8_e32 v65, v161, v189
	v_dot4c_i32_i8_e32 v35, v165, v189
	s_waitcnt vmcnt(4)
	v_dot4c_i32_i8_e32 v34, v166, v186
	v_dot4c_i32_i8_e32 v34, v167, v187
	s_waitcnt vmcnt(3)
	v_dot4c_i32_i8_e32 v25, v170, v186
	v_dot4c_i32_i8_e32 v25, v171, v187
	s_waitcnt vmcnt(2)
	v_dot4c_i32_i8_e32 v29, v174, v186
	v_dot4c_i32_i8_e32 v29, v175, v187
	s_waitcnt vmcnt(1)
	v_dot4c_i32_i8_e32 v27, v178, v186
	v_dot4c_i32_i8_e32 v27, v179, v187
	s_waitcnt vmcnt(0)
	v_dot4c_i32_i8_e32 v9, v182, v186
	v_dot4c_i32_i8_e32 v9, v183, v187
	v_dot4c_i32_i8_e32 v34, v168, v188
	v_dot4c_i32_i8_e32 v25, v172, v188
	v_dot4c_i32_i8_e32 v29, v176, v188
	v_dot4c_i32_i8_e32 v27, v180, v188
	v_dot4c_i32_i8_e32 v9, v184, v188
	v_dot4c_i32_i8_e32 v34, v169, v189
	v_dot4c_i32_i8_e32 v25, v173, v189
	v_dot4c_i32_i8_e32 v29, v177, v189
	v_dot4c_i32_i8_e32 v27, v181, v189
	v_dot4c_i32_i8_e32 v9, v185, v189
	s_addk_i32 s50, 0x80
	s_cmpk_eq_i32 s50, 0x1000
	s_cbranch_scc0 .LBB0_1206
	v_cvt_f32_i32_e32 v120, v120
	v_cvt_f32_i32_e32 v119, v119
	v_cvt_f32_i32_e32 v123, v33
	v_mul_f32_e32 v33, 0x3c010204, v5
	ds_bpermute_b32 v121, v41, v120
	ds_bpermute_b32 v122, v41, v119
	v_cvt_f32_i32_e32 v5, v118
	ds_bpermute_b32 v118, v41, v123
	v_cvt_f32_i32_e32 v116, v116
	s_waitcnt lgkmcnt(2)
	v_add_f32_e32 v120, v120, v121
	s_waitcnt lgkmcnt(1)
	v_add_f32_e32 v119, v119, v122
	ds_bpermute_b32 v121, v40, v120
	ds_bpermute_b32 v122, v40, v119
	ds_bpermute_b32 v124, v41, v5
	s_waitcnt lgkmcnt(3)
	v_add_f32_e32 v118, v123, v118
	ds_bpermute_b32 v123, v40, v118
	s_waitcnt lgkmcnt(3)
	v_add_f32_e32 v120, v120, v121
	s_waitcnt lgkmcnt(2)
	v_add_f32_e32 v119, v119, v122
	ds_bpermute_b32 v121, v39, v120
	ds_bpermute_b32 v122, v39, v119
	s_waitcnt lgkmcnt(3)
	v_add_f32_e32 v5, v5, v124
	s_waitcnt lgkmcnt(2)
	v_add_f32_e32 v118, v118, v123
	v_cvt_f32_i32_e32 v117, v117
	s_waitcnt lgkmcnt(1)
	v_add_f32_e32 v120, v120, v121
	s_waitcnt lgkmcnt(0)
	v_add_f32_e32 v119, v119, v122
	ds_bpermute_b32 v120, v44, v120
	ds_bpermute_b32 v122, v40, v5
	ds_bpermute_b32 v119, v44, v119
	ds_bpermute_b32 v121, v39, v118
	ds_bpermute_b32 v123, v41, v117
	s_waitcnt lgkmcnt(4)
	v_cndmask_b32_e64 v120, 0, v120, s[10:11]
	s_waitcnt lgkmcnt(3)
	v_add_f32_e32 v5, v5, v122
	s_waitcnt lgkmcnt(2)
	v_cndmask_b32_e64 v119, v120, v119, s[12:13]
	ds_bpermute_b32 v120, v39, v5
	s_waitcnt lgkmcnt(2)
	v_add_f32_e32 v118, v118, v121
	ds_bpermute_b32 v118, v44, v118
	s_waitcnt lgkmcnt(2)
	v_add_f32_e32 v117, v117, v123
	ds_bpermute_b32 v121, v40, v117
	s_waitcnt lgkmcnt(2)
	v_add_f32_e32 v5, v5, v120
	ds_bpermute_b32 v120, v41, v116
	ds_bpermute_b32 v5, v44, v5
	s_waitcnt lgkmcnt(3)
; __device__ __forceinline__ void peer_expert_phase(const Args& a, int layer, LAS unsigned char* lds, int G, int bid) {
;     ...
;         float pa[4], pb[4];
; #pragma unroll
;         for (int i = 0; i < 4; ++i) { pa[i] = 0.f; pb[i] = 0.f;
; #pragma unroll
;             for (int c = 0; c < 16; ++c) { float v = (float)pacc[i][c]; v += __shfl_xor(v, 1); v += __shfl_xor(v, 2); v += __shfl_xor(v, 4);
;                 const float t = __shfl(v, 8 * (lane & 7));
;                 if (c < 8) pa[i] = (g8 == c) ? t : pa[i]; else pb[i] = (g8 == c - 8) ? t : pb[i]; } }
	v_cndmask_b32_e64 v118, v119, v118, s[14:15]
	v_cvt_f32_i32_e32 v114, v114
	s_waitcnt lgkmcnt(2)
	v_add_f32_e32 v117, v117, v121
	s_waitcnt lgkmcnt(1)
	v_add_f32_e32 v116, v116, v120
	ds_bpermute_b32 v120, v40, v116
	s_waitcnt lgkmcnt(1)
	v_cndmask_b32_e64 v5, v118, v5, s[16:17]
	v_cvt_f32_i32_e32 v115, v115
	ds_bpermute_b32 v121, v39, v117
	v_cvt_f32_i32_e32 v113, v113
	s_waitcnt lgkmcnt(1)
	v_add_f32_e32 v116, v116, v120
	ds_bpermute_b32 v118, v39, v116
	ds_bpermute_b32 v119, v41, v115
	s_waitcnt lgkmcnt(2)
	v_add_f32_e32 v117, v117, v121
	ds_bpermute_b32 v117, v44, v117
	v_cvt_f32_i32_e32 v112, v112
	s_waitcnt lgkmcnt(2)
	v_add_f32_e32 v116, v116, v118
	ds_bpermute_b32 v118, v41, v114
	ds_bpermute_b32 v116, v44, v116
	s_waitcnt lgkmcnt(3)
	v_add_f32_e32 v115, v115, v119
	ds_bpermute_b32 v119, v40, v115
	s_waitcnt lgkmcnt(3)
	v_cndmask_b32_e64 v5, v5, v117, s[18:19]
	s_waitcnt lgkmcnt(2)
	v_add_f32_e32 v114, v114, v118
	ds_bpermute_b32 v118, v40, v114
	ds_bpermute_b32 v117, v41, v113
	s_waitcnt lgkmcnt(3)
	v_cndmask_b32_e64 v5, v5, v116, s[20:21]
	s_waitcnt lgkmcnt(2)
	v_add_f32_e32 v115, v115, v119
	ds_bpermute_b32 v119, v39, v115
	s_waitcnt lgkmcnt(2)
	v_add_f32_e32 v114, v114, v118
	ds_bpermute_b32 v116, v39, v114
	s_waitcnt lgkmcnt(2)
	v_add_f32_e32 v113, v113, v117
	ds_bpermute_b32 v117, v40, v113
	s_waitcnt lgkmcnt(2)
	v_add_f32_e32 v115, v115, v119
	ds_bpermute_b32 v115, v44, v115
	s_waitcnt lgkmcnt(2)
	v_add_f32_e32 v114, v114, v116
	ds_bpermute_b32 v116, v41, v112
	v_cvt_f32_i32_e32 v118, v32
	s_waitcnt lgkmcnt(2)
	v_add_f32_e32 v113, v113, v117
	ds_bpermute_b32 v114, v44, v114
	ds_bpermute_b32 v117, v39, v113
	s_waitcnt lgkmcnt(2)
	v_add_f32_e32 v112, v112, v116
	ds_bpermute_b32 v116, v40, v112
	v_cndmask_b32_e64 v5, v5, v115, s[22:23]
	ds_bpermute_b32 v115, v41, v118
	s_waitcnt lgkmcnt(3)
	v_cndmask_b32_e64 v32, v5, v114, s[24:25]
	s_waitcnt lgkmcnt(2)
	v_add_f32_e32 v5, v113, v117
	s_waitcnt lgkmcnt(1)
	v_add_f32_e32 v112, v112, v116
	ds_bpermute_b32 v113, v39, v112
	s_waitcnt lgkmcnt(1)
	v_add_f32_e32 v114, v118, v115
	ds_bpermute_b32 v115, v40, v114
	v_cvt_f32_i32_e32 v116, v111
	ds_bpermute_b32 v111, v44, v5
	s_waitcnt lgkmcnt(2)
	v_add_f32_e32 v5, v112, v113
	v_cvt_f32_i32_e32 v112, v110
	ds_bpermute_b32 v113, v41, v116
	s_waitcnt lgkmcnt(2)
	v_add_f32_e32 v114, v114, v115
	ds_bpermute_b32 v115, v39, v114
	ds_bpermute_b32 v117, v41, v112
	ds_bpermute_b32 v110, v44, v5
	s_waitcnt lgkmcnt(3)
	v_add_f32_e32 v5, v116, v113
	ds_bpermute_b32 v113, v40, v5
	s_waitcnt lgkmcnt(3)
	v_add_f32_e32 v114, v114, v115
	s_waitcnt lgkmcnt(2)
	v_add_f32_e32 v115, v112, v117
	ds_bpermute_b32 v116, v40, v115
	v_cvt_f32_i32_e32 v109, v109
	s_waitcnt lgkmcnt(1)
	v_add_f32_e32 v5, v5, v113
	ds_bpermute_b32 v112, v44, v114
	ds_bpermute_b32 v113, v39, v5
	s_waitcnt lgkmcnt(2)
	v_add_f32_e32 v114, v115, v116
	ds_bpermute_b32 v117, v41, v109
	ds_bpermute_b32 v116, v39, v114
	v_cvt_f32_i32_e32 v108, v108
	s_waitcnt lgkmcnt(2)
	v_add_f32_e32 v5, v5, v113
	ds_bpermute_b32 v115, v44, v5
	s_waitcnt lgkmcnt(2)
	v_add_f32_e32 v109, v109, v117
	ds_bpermute_b32 v113, v41, v108
	s_waitcnt lgkmcnt(2)
	v_add_f32_e32 v5, v114, v116
	ds_bpermute_b32 v114, v40, v109
	v_cvt_f32_i32_e32 v107, v107
	ds_bpermute_b32 v119, v44, v5
	s_waitcnt lgkmcnt(2)
	v_add_f32_e32 v108, v108, v113
	ds_bpermute_b32 v113, v40, v108
	s_waitcnt lgkmcnt(2)
	v_add_f32_e32 v5, v109, v114
	ds_bpermute_b32 v109, v41, v107
	ds_bpermute_b32 v114, v39, v5
	v_cvt_f32_i32_e32 v106, v106
	s_waitcnt lgkmcnt(2)
	v_add_f32_e32 v108, v108, v113
	ds_bpermute_b32 v113, v39, v108
	s_waitcnt lgkmcnt(2)
	v_add_f32_e32 v107, v107, v109
	ds_bpermute_b32 v109, v40, v107
	s_waitcnt lgkmcnt(2)
	v_add_f32_e32 v5, v5, v114
	ds_bpermute_b32 v114, v41, v106
	ds_bpermute_b32 v120, v44, v5
	s_waitcnt lgkmcnt(3)
	v_add_f32_e32 v5, v108, v113
	s_waitcnt lgkmcnt(2)
	v_add_f32_e32 v107, v107, v109
	ds_bpermute_b32 v108, v39, v107
	s_waitcnt lgkmcnt(2)
	v_add_f32_e32 v106, v106, v114
	v_cvt_f32_i32_e32 v105, v105
	ds_bpermute_b32 v109, v40, v106
	v_cvt_f32_i32_e32 v104, v104
	ds_bpermute_b32 v121, v44, v5
	s_waitcnt lgkmcnt(2)
	v_add_f32_e32 v5, v107, v108
	ds_bpermute_b32 v107, v41, v105
	s_waitcnt lgkmcnt(2)
	v_add_f32_e32 v106, v106, v109
	ds_bpermute_b32 v109, v41, v104
	ds_bpermute_b32 v108, v39, v106
	ds_bpermute_b32 v122, v44, v5
	s_waitcnt lgkmcnt(3)
	v_add_f32_e32 v5, v105, v107
	ds_bpermute_b32 v105, v40, v5
	s_waitcnt lgkmcnt(3)
	v_add_f32_e32 v107, v104, v109
	s_waitcnt lgkmcnt(2)
	v_add_f32_e32 v106, v106, v108
	ds_bpermute_b32 v108, v40, v107
	v_cvt_f32_i32_e32 v103, v103
	s_waitcnt lgkmcnt(1)
	v_add_f32_e32 v5, v5, v105
	ds_bpermute_b32 v105, v39, v5
	ds_bpermute_b32 v104, v44, v106
	s_waitcnt lgkmcnt(2)
	v_add_f32_e32 v106, v107, v108
	v_cvt_f32_i32_e32 v107, v102
	ds_bpermute_b32 v109, v41, v103
	ds_bpermute_b32 v108, v39, v106
	s_waitcnt lgkmcnt(3)
	v_add_f32_e32 v5, v5, v105
	ds_bpermute_b32 v105, v41, v107
	ds_bpermute_b32 v102, v44, v5
	s_waitcnt lgkmcnt(3)
	v_add_f32_e32 v103, v103, v109
	s_waitcnt lgkmcnt(2)
	v_add_f32_e32 v5, v106, v108
	ds_bpermute_b32 v106, v40, v103
	s_waitcnt lgkmcnt(2)
	v_add_f32_e32 v105, v107, v105
	v_cvt_f32_i32_e32 v107, v101
	ds_bpermute_b32 v101, v44, v5
	ds_bpermute_b32 v108, v40, v105
	s_waitcnt lgkmcnt(2)
	v_add_f32_e32 v5, v103, v106
	ds_bpermute_b32 v103, v41, v107
	ds_bpermute_b32 v106, v39, v5
	v_cvt_f32_i32_e32 v109, v100
	s_waitcnt lgkmcnt(2)
	v_add_f32_e32 v105, v105, v108
	ds_bpermute_b32 v108, v39, v105
	s_waitcnt lgkmcnt(2)
	v_add_f32_e32 v103, v107, v103
	ds_bpermute_b32 v107, v40, v103
	s_waitcnt lgkmcnt(2)
; __device__ __forceinline__ void peer_expert_phase(const Args& a, int layer, LAS unsigned char* lds, int G, int bid) {
;     ...
;         float pa[4], pb[4];
; #pragma unroll
;         for (int i = 0; i < 4; ++i) { pa[i] = 0.f; pb[i] = 0.f;
; #pragma unroll
;             for (int c = 0; c < 16; ++c) { float v = (float)pacc[i][c]; v += __shfl_xor(v, 1); v += __shfl_xor(v, 2); v += __shfl_xor(v, 4);
;                 const float t = __shfl(v, 8 * (lane & 7));
;                 if (c < 8) pa[i] = (g8 == c) ? t : pa[i]; else pb[i] = (g8 == c - 8) ? t : pb[i]; } }
	v_add_f32_e32 v5, v5, v106
	ds_bpermute_b32 v106, v41, v109
	ds_bpermute_b32 v100, v44, v5
	s_waitcnt lgkmcnt(3)
	v_add_f32_e32 v5, v105, v108
	s_waitcnt lgkmcnt(2)
	v_add_f32_e32 v103, v103, v107
	ds_bpermute_b32 v105, v39, v103
	v_cvt_f32_i32_e32 v108, v99
	s_waitcnt lgkmcnt(2)
	v_add_f32_e32 v106, v109, v106
	ds_bpermute_b32 v107, v40, v106
	ds_bpermute_b32 v99, v44, v5
	s_waitcnt lgkmcnt(2)
	v_add_f32_e32 v5, v103, v105
	v_cvt_f32_i32_e32 v98, v98
	ds_bpermute_b32 v103, v41, v108
	s_waitcnt lgkmcnt(2)
	v_add_f32_e32 v105, v106, v107
	ds_bpermute_b32 v106, v39, v105
	ds_bpermute_b32 v109, v41, v98
	ds_bpermute_b32 v107, v44, v5
	s_waitcnt lgkmcnt(3)
	v_add_f32_e32 v5, v108, v103
	ds_bpermute_b32 v103, v40, v5
	s_waitcnt lgkmcnt(3)
	v_add_f32_e32 v105, v105, v106
	s_waitcnt lgkmcnt(2)
	v_add_f32_e32 v98, v98, v109
	ds_bpermute_b32 v106, v40, v98
	v_cvt_f32_i32_e32 v97, v97
	s_waitcnt lgkmcnt(1)
	v_add_f32_e32 v5, v5, v103
	ds_bpermute_b32 v103, v39, v5
	v_cvt_f32_i32_e32 v96, v96
	s_waitcnt lgkmcnt(1)
	v_add_f32_e32 v98, v98, v106
	ds_bpermute_b32 v106, v41, v97
	ds_bpermute_b32 v109, v44, v105
	ds_bpermute_b32 v105, v39, v98
	s_waitcnt lgkmcnt(3)
	v_add_f32_e32 v5, v5, v103
	ds_bpermute_b32 v103, v41, v96
	s_waitcnt lgkmcnt(3)
	v_add_f32_e32 v97, v97, v106
	ds_bpermute_b32 v113, v44, v5
	s_waitcnt lgkmcnt(2)
	v_add_f32_e32 v5, v98, v105
	ds_bpermute_b32 v98, v40, v97
	s_waitcnt lgkmcnt(2)
	v_add_f32_e32 v96, v96, v103
	v_cvt_f32_i32_e32 v103, v93
	ds_bpermute_b32 v105, v40, v96
	ds_bpermute_b32 v93, v44, v5
	s_waitcnt lgkmcnt(2)
	v_add_f32_e32 v5, v97, v98
	ds_bpermute_b32 v97, v41, v103
	ds_bpermute_b32 v98, v39, v5
	s_waitcnt lgkmcnt(3)
	v_add_f32_e32 v96, v96, v105
	v_cvt_f32_i32_e32 v106, v95
	ds_bpermute_b32 v105, v39, v96
	s_waitcnt lgkmcnt(2)
	v_add_f32_e32 v97, v103, v97
	ds_bpermute_b32 v103, v40, v97
	s_waitcnt lgkmcnt(2)
	v_add_f32_e32 v5, v5, v98
	ds_bpermute_b32 v98, v41, v106
	ds_bpermute_b32 v95, v44, v5
	s_waitcnt lgkmcnt(3)
	v_add_f32_e32 v5, v96, v105
	s_waitcnt lgkmcnt(2)
	v_add_f32_e32 v96, v97, v103
	ds_bpermute_b32 v97, v39, v96
	s_waitcnt lgkmcnt(2)
	v_add_f32_e32 v98, v106, v98
	ds_bpermute_b32 v103, v40, v98
	v_cvt_f32_i32_e32 v105, v94
	ds_bpermute_b32 v94, v44, v5
	s_waitcnt lgkmcnt(2)
	v_add_f32_e32 v5, v96, v97
	v_cvt_f32_i32_e32 v96, v92
	ds_bpermute_b32 v97, v41, v105
	s_waitcnt lgkmcnt(2)
	v_add_f32_e32 v98, v98, v103
	ds_bpermute_b32 v103, v39, v98
	ds_bpermute_b32 v106, v41, v96
	ds_bpermute_b32 v92, v44, v5
	s_waitcnt lgkmcnt(3)
	v_add_f32_e32 v5, v105, v97
	ds_bpermute_b32 v97, v40, v5
	s_waitcnt lgkmcnt(3)
	v_add_f32_e32 v98, v98, v103
	s_waitcnt lgkmcnt(2)
	v_add_f32_e32 v103, v96, v106
	ds_bpermute_b32 v105, v40, v103
	v_cvt_f32_i32_e32 v91, v91
	s_waitcnt lgkmcnt(1)
	v_add_f32_e32 v5, v5, v97
	ds_bpermute_b32 v96, v44, v98
	ds_bpermute_b32 v97, v39, v5
	s_waitcnt lgkmcnt(2)
	v_add_f32_e32 v98, v103, v105
	ds_bpermute_b32 v105, v41, v91
	ds_bpermute_b32 v103, v39, v98
	v_cvt_f32_i32_e32 v90, v90
	s_waitcnt lgkmcnt(2)
	v_add_f32_e32 v5, v5, v97
	ds_bpermute_b32 v108, v44, v5
	s_waitcnt lgkmcnt(2)
	v_add_f32_e32 v91, v91, v105
	ds_bpermute_b32 v97, v41, v90
	s_waitcnt lgkmcnt(2)
	v_add_f32_e32 v5, v98, v103
	ds_bpermute_b32 v98, v40, v91
	v_cvt_f32_i32_e32 v89, v89
	ds_bpermute_b32 v114, v44, v5
	s_waitcnt lgkmcnt(2)
	v_add_f32_e32 v90, v90, v97
	ds_bpermute_b32 v97, v40, v90
	s_waitcnt lgkmcnt(2)
	v_add_f32_e32 v5, v91, v98
	ds_bpermute_b32 v91, v41, v89
	ds_bpermute_b32 v98, v39, v5
	v_cvt_f32_i32_e32 v88, v88
	s_waitcnt lgkmcnt(2)
	v_add_f32_e32 v90, v90, v97
	ds_bpermute_b32 v97, v39, v90
	s_waitcnt lgkmcnt(2)
	v_add_f32_e32 v89, v89, v91
	ds_bpermute_b32 v91, v40, v89
	s_waitcnt lgkmcnt(2)
	v_add_f32_e32 v5, v5, v98
	ds_bpermute_b32 v98, v41, v88
	ds_bpermute_b32 v116, v44, v5
	s_waitcnt lgkmcnt(3)
	v_add_f32_e32 v5, v90, v97
	s_waitcnt lgkmcnt(2)
	v_add_f32_e32 v89, v89, v91
	ds_bpermute_b32 v90, v39, v89
	s_waitcnt lgkmcnt(2)
	v_add_f32_e32 v88, v88, v98
	v_cvt_f32_i32_e32 v97, v87
	ds_bpermute_b32 v91, v40, v88
	ds_bpermute_b32 v87, v44, v5
	s_waitcnt lgkmcnt(2)
	v_add_f32_e32 v5, v89, v90
	v_cvt_f32_i32_e32 v89, v86
	ds_bpermute_b32 v90, v41, v97
	s_waitcnt lgkmcnt(2)
	v_add_f32_e32 v88, v88, v91
	ds_bpermute_b32 v91, v39, v88
	ds_bpermute_b32 v98, v41, v89
	ds_bpermute_b32 v86, v44, v5
	s_waitcnt lgkmcnt(3)
	v_add_f32_e32 v5, v97, v90
	ds_bpermute_b32 v90, v40, v5
	s_waitcnt lgkmcnt(3)
	v_add_f32_e32 v88, v88, v91
	s_waitcnt lgkmcnt(2)
	v_add_f32_e32 v89, v89, v98
	ds_bpermute_b32 v91, v40, v89
	v_cvt_f32_i32_e32 v85, v85
	s_waitcnt lgkmcnt(1)
	v_add_f32_e32 v5, v5, v90
	ds_bpermute_b32 v90, v39, v5
	v_cvt_f32_i32_e32 v80, v80
	s_waitcnt lgkmcnt(1)
	v_add_f32_e32 v89, v89, v91
	v_cvt_f32_i32_e32 v91, v84
	ds_bpermute_b32 v98, v41, v85
	ds_bpermute_b32 v97, v39, v89
	s_waitcnt lgkmcnt(2)
	v_add_f32_e32 v5, v5, v90
	ds_bpermute_b32 v90, v41, v91
	ds_bpermute_b32 v84, v44, v5
	s_waitcnt lgkmcnt(3)
	v_add_f32_e32 v85, v85, v98
	s_waitcnt lgkmcnt(2)
	v_add_f32_e32 v5, v89, v97
	ds_bpermute_b32 v89, v40, v85
	s_waitcnt lgkmcnt(2)
	v_add_f32_e32 v90, v91, v90
	v_cvt_f32_i32_e32 v91, v83
	ds_bpermute_b32 v97, v40, v90
	ds_bpermute_b32 v83, v44, v5
	s_waitcnt lgkmcnt(2)
	v_add_f32_e32 v5, v85, v89
	ds_bpermute_b32 v85, v41, v91
	ds_bpermute_b32 v89, v39, v5
	v_cvt_f32_i32_e32 v98, v82
	s_waitcnt lgkmcnt(3)
	v_add_f32_e32 v90, v90, v97
	ds_bpermute_b32 v97, v39, v90
	s_waitcnt lgkmcnt(2)
	v_add_f32_e32 v85, v91, v85
	ds_bpermute_b32 v91, v40, v85
	s_waitcnt lgkmcnt(2)
	v_add_f32_e32 v5, v5, v89
	ds_bpermute_b32 v89, v41, v98
	ds_bpermute_b32 v82, v44, v5
	s_waitcnt lgkmcnt(3)
; __device__ __forceinline__ void peer_expert_phase(const Args& a, int layer, LAS unsigned char* lds, int G, int bid) {
;     ...
;         float pa[4], pb[4];
; #pragma unroll
;         for (int i = 0; i < 4; ++i) { pa[i] = 0.f; pb[i] = 0.f;
; #pragma unroll
;             for (int c = 0; c < 16; ++c) { float v = (float)pacc[i][c]; v += __shfl_xor(v, 1); v += __shfl_xor(v, 2); v += __shfl_xor(v, 4);
;                 const float t = __shfl(v, 8 * (lane & 7));
;                 if (c < 8) pa[i] = (g8 == c) ? t : pa[i]; else pb[i] = (g8 == c - 8) ? t : pb[i]; } }
;         float wa[4], wb[4], ssq[4], hgm[4] = {0.f, 0.f, 0.f, 0.f};
; #pragma unroll
;         for (int i = 0; i < 4; ++i) { int tok = tb + i * NGW; tok = tok < NTOK ? tok : tb;
;             const float rstd_t = 1.0f / sqrtf(wave_sum(((const float*)(ws + WS_SSP))[((size_t)layer * NTOK + tok) * 64 + lane]) * (1.0f / DM) + EPS);
	v_add_f32_e32 v5, v90, v97
	s_waitcnt lgkmcnt(2)
	v_add_f32_e32 v90, v85, v91
	ds_bpermute_b32 v91, v39, v90
	s_waitcnt lgkmcnt(2)
	v_add_f32_e32 v89, v98, v89
	ds_bpermute_b32 v97, v40, v89
	v_cvt_f32_i32_e32 v98, v81
	ds_bpermute_b32 v85, v44, v5
	s_waitcnt lgkmcnt(2)
	v_add_f32_e32 v5, v90, v91
	ds_bpermute_b32 v81, v44, v5
	ds_bpermute_b32 v90, v41, v98
	s_waitcnt lgkmcnt(3)
	v_add_f32_e32 v89, v89, v97
	ds_bpermute_b32 v91, v39, v89
	ds_bpermute_b32 v97, v41, v80
	v_cvt_f32_i32_e32 v79, v79
	s_waitcnt lgkmcnt(2)
	v_add_f32_e32 v5, v98, v90
	ds_bpermute_b32 v90, v40, v5
	s_waitcnt lgkmcnt(2)
	v_add_f32_e32 v89, v89, v91
	s_waitcnt lgkmcnt(1)
	v_add_f32_e32 v91, v80, v97
	ds_bpermute_b32 v97, v40, v91
	ds_bpermute_b32 v80, v44, v89
	s_waitcnt lgkmcnt(2)
	v_add_f32_e32 v5, v5, v90
	ds_bpermute_b32 v89, v39, v5
	ds_bpermute_b32 v98, v41, v79
	s_waitcnt lgkmcnt(3)
	v_add_f32_e32 v90, v91, v97
	v_cvt_f32_i32_e32 v91, v78
	ds_bpermute_b32 v97, v39, v90
	s_waitcnt lgkmcnt(2)
	v_add_f32_e32 v5, v5, v89
	s_waitcnt lgkmcnt(1)
	v_add_f32_e32 v79, v79, v98
	ds_bpermute_b32 v89, v41, v91
	ds_bpermute_b32 v78, v44, v5
	s_waitcnt lgkmcnt(2)
	v_add_f32_e32 v5, v90, v97
	ds_bpermute_b32 v90, v40, v79
	v_cvt_f32_i32_e32 v98, v76
	s_waitcnt lgkmcnt(2)
	v_add_f32_e32 v89, v91, v89
	v_cvt_f32_i32_e32 v91, v77
	ds_bpermute_b32 v77, v44, v5
	s_waitcnt lgkmcnt(1)
	v_add_f32_e32 v5, v79, v90
	ds_bpermute_b32 v97, v40, v89
	ds_bpermute_b32 v79, v41, v91
	ds_bpermute_b32 v90, v39, v5
	v_cvt_f32_i32_e32 v73, v73
	v_cvt_f32_i32_e32 v72, v72
	s_waitcnt lgkmcnt(2)
	v_add_f32_e32 v89, v89, v97
	s_waitcnt lgkmcnt(1)
	v_add_f32_e32 v79, v91, v79
	ds_bpermute_b32 v91, v40, v79
	ds_bpermute_b32 v97, v39, v89
	s_waitcnt lgkmcnt(2)
	v_add_f32_e32 v5, v5, v90
	ds_bpermute_b32 v90, v41, v98
	ds_bpermute_b32 v76, v44, v5
	s_waitcnt lgkmcnt(3)
	v_add_f32_e32 v79, v79, v91
	s_waitcnt lgkmcnt(2)
	v_add_f32_e32 v5, v89, v97
	ds_bpermute_b32 v89, v39, v79
	v_cvt_f32_i32_e32 v97, v75
	s_waitcnt lgkmcnt(2)
	v_add_f32_e32 v90, v98, v90
	ds_bpermute_b32 v75, v44, v5
	ds_bpermute_b32 v91, v40, v90
	s_waitcnt lgkmcnt(2)
	v_add_f32_e32 v5, v79, v89
	ds_bpermute_b32 v89, v41, v97
	v_cvt_f32_i32_e32 v79, v74
	ds_bpermute_b32 v74, v44, v5
	s_waitcnt lgkmcnt(2)
	v_add_f32_e32 v90, v90, v91
	ds_bpermute_b32 v91, v39, v90
	s_waitcnt lgkmcnt(2)
	v_add_f32_e32 v5, v97, v89
	ds_bpermute_b32 v89, v40, v5
	ds_bpermute_b32 v98, v41, v79
	s_lshl_b64 s[34:35], s[38:39], 8
	s_waitcnt lgkmcnt(2)
	v_add_f32_e32 v90, v90, v91
	v_cvt_f32_i32_e32 v105, v70
	s_waitcnt lgkmcnt(1)
	v_add_f32_e32 v5, v5, v89
	s_waitcnt lgkmcnt(0)
	v_add_f32_e32 v91, v79, v98
	ds_bpermute_b32 v89, v39, v5
	ds_bpermute_b32 v97, v40, v91
	ds_bpermute_b32 v79, v44, v90
	ds_bpermute_b32 v98, v41, v73
	v_cvt_f32_i32_e32 v68, v68
	s_waitcnt lgkmcnt(3)
	v_add_f32_e32 v5, v5, v89
	s_waitcnt lgkmcnt(2)
	v_add_f32_e32 v91, v91, v97
	ds_bpermute_b32 v90, v44, v5
	ds_bpermute_b32 v5, v41, v72
	ds_bpermute_b32 v97, v39, v91
	s_waitcnt lgkmcnt(3)
	v_add_f32_e32 v73, v73, v98
	v_cvt_f32_i32_e32 v67, v67
	v_cvt_f32_i32_e32 v66, v66
	s_waitcnt lgkmcnt(1)
	v_add_f32_e32 v5, v72, v5
	s_waitcnt lgkmcnt(0)
	v_add_f32_e32 v89, v91, v97
	ds_bpermute_b32 v91, v40, v73
	ds_bpermute_b32 v72, v40, v5
	v_cvt_f32_i32_e32 v97, v71
	ds_bpermute_b32 v71, v44, v89
	v_cvt_f32_i32_e32 v65, v65
	s_waitcnt lgkmcnt(2)
	v_add_f32_e32 v91, v73, v91
	s_waitcnt lgkmcnt(1)
	v_add_f32_e32 v5, v5, v72
	v_lshl_add_u64 v[72:73], v[16:17], 0, s[34:35]
	global_load_dword v106, v[72:73], off
	ds_bpermute_b32 v89, v41, v97
	ds_bpermute_b32 v72, v41, v105
	ds_bpermute_b32 v98, v39, v91
	ds_bpermute_b32 v103, v39, v5
	v_cvt_f32_i32_e32 v35, v35
	s_waitcnt lgkmcnt(3)
	v_add_f32_e32 v89, v97, v89
	ds_bpermute_b32 v97, v40, v89
	s_waitcnt lgkmcnt(3)
	v_add_f32_e32 v72, v105, v72
	s_waitcnt lgkmcnt(2)
	v_add_f32_e32 v70, v91, v98
	ds_bpermute_b32 v91, v40, v72
	s_waitcnt lgkmcnt(2)
	v_add_f32_e32 v5, v5, v103
	s_waitcnt lgkmcnt(1)
	v_add_f32_e32 v73, v89, v97
	ds_bpermute_b32 v89, v39, v73
	v_cvt_f32_i32_e32 v97, v69
	ds_bpermute_b32 v69, v44, v5
	s_waitcnt lgkmcnt(2)
	v_add_f32_e32 v72, v72, v91
	ds_bpermute_b32 v98, v41, v68
	s_waitcnt lgkmcnt(2)
	v_add_f32_e32 v5, v73, v89
	ds_bpermute_b32 v73, v41, v97
	ds_bpermute_b32 v91, v39, v72
	ds_bpermute_b32 v89, v44, v5
	s_waitcnt lgkmcnt(3)
	v_add_f32_e32 v68, v68, v98
	ds_bpermute_b32 v98, v41, v67
	s_waitcnt lgkmcnt(3)
	v_add_f32_e32 v5, v97, v73
	ds_bpermute_b32 v97, v40, v5
	s_waitcnt lgkmcnt(3)
	v_add_f32_e32 v72, v72, v91
	ds_bpermute_b32 v91, v40, v68
	ds_bpermute_b32 v73, v44, v72
	s_waitcnt lgkmcnt(3)
	v_add_f32_e32 v67, v67, v98
	s_waitcnt lgkmcnt(2)
	v_add_f32_e32 v5, v5, v97
	ds_bpermute_b32 v72, v39, v5
	s_waitcnt lgkmcnt(2)
	v_add_f32_e32 v68, v68, v91
	ds_bpermute_b32 v91, v39, v68
	v_cvt_f32_i32_e32 v34, v34
	v_lshl_add_u64 v[124:125], v[18:19], 0, s[28:29]
	s_waitcnt lgkmcnt(1)
	v_add_f32_e32 v5, v5, v72
	ds_bpermute_b32 v72, v41, v66
	ds_bpermute_b32 v97, v44, v5
	s_waitcnt lgkmcnt(2)
	v_add_f32_e32 v5, v68, v91
	ds_bpermute_b32 v68, v40, v67
	ds_bpermute_b32 v103, v44, v5
	s_waitcnt lgkmcnt(3)
; __device__ __forceinline__ float gelu_tanh(float x) { const float u = 0.7978845608028654f * (x + 0.044715f * x * x * x); return 0.5f * x * (1.0f + tanhf(u)); }
; __device__ __forceinline__ void peer_expert_phase(const Args& a, int layer, LAS unsigned char* lds, int G, int bid) {
;     ...
;         float pa[4], pb[4];
; #pragma unroll
;         for (int i = 0; i < 4; ++i) { pa[i] = 0.f; pb[i] = 0.f;
; #pragma unroll
;             for (int c = 0; c < 16; ++c) { float v = (float)pacc[i][c]; v += __shfl_xor(v, 1); v += __shfl_xor(v, 2); v += __shfl_xor(v, 4);
;                 const float t = __shfl(v, 8 * (lane & 7));
;                 if (c < 8) pa[i] = (g8 == c) ? t : pa[i]; else pb[i] = (g8 == c - 8) ? t : pb[i]; } }
;         float wa[4], wb[4], ssq[4], hgm[4] = {0.f, 0.f, 0.f, 0.f};
; #pragma unroll
;         for (int i = 0; i < 4; ++i) { int tok = tb + i * NGW; tok = tok < NTOK ? tok : tb;
;             const float rstd_t = 1.0f / sqrtf(wave_sum(((const float*)(ws + WS_SSP))[((size_t)layer * NTOK + tok) * 64 + lane]) * (1.0f / DM) + EPS);
;             const float ga = GATE[(size_t)tok * 128 + lane], gb = GATE[(size_t)tok * 128 + 64 + lane];
;             const float rx = rstd_t * xs[i];
;             wa[i] = ga * gelu_tanh(pa[i] * SCU[ea[i]] * rx) * SCV[ea[i]]; wb[i] = gb * gelu_tanh(pb[i] * SCU[eb[i]] * rx) * SCV[eb[i]]; ssq[i] = 0.f; }
	v_add_f32_e32 v66, v66, v72
	ds_bpermute_b32 v72, v40, v66
	v_cvt_f32_i32_e32 v29, v29
	s_waitcnt lgkmcnt(2)
	v_add_f32_e32 v5, v67, v68
	ds_bpermute_b32 v67, v41, v65
	ds_bpermute_b32 v68, v39, v5
	s_waitcnt lgkmcnt(2)
	v_add_f32_e32 v66, v66, v72
	ds_bpermute_b32 v72, v39, v66
	v_cvt_f32_i32_e32 v27, v27
	s_waitcnt lgkmcnt(2)
	v_add_f32_e32 v65, v65, v67
	ds_bpermute_b32 v67, v40, v65
	s_waitcnt lgkmcnt(2)
	v_add_f32_e32 v5, v5, v68
	ds_bpermute_b32 v68, v41, v35
	ds_bpermute_b32 v98, v44, v5
	s_waitcnt lgkmcnt(3)
	v_add_f32_e32 v5, v66, v72
	s_waitcnt lgkmcnt(2)
	v_add_f32_e32 v66, v65, v67
	ds_bpermute_b32 v67, v39, v66
	s_waitcnt lgkmcnt(2)
	v_add_f32_e32 v35, v35, v68
	ds_bpermute_b32 v68, v40, v35
	ds_bpermute_b32 v65, v44, v5
	v_cvt_f32_i32_e32 v9, v9
	s_waitcnt lgkmcnt(2)
	v_add_f32_e32 v5, v66, v67
	ds_bpermute_b32 v67, v41, v34
	ds_bpermute_b32 v66, v44, v5
	s_waitcnt lgkmcnt(3)
	v_add_f32_e32 v5, v35, v68
	v_cvt_f32_i32_e32 v68, v25
	v_ashrrev_i32_e32 v25, 31, v24
	s_waitcnt lgkmcnt(1)
	v_add_f32_e32 v67, v34, v67
	v_lshl_add_u64 v[126:127], v[24:25], 2, s[42:43]
	global_load_dword v34, v[124:125], off
	global_load_dword v35, v[124:125], off offset:256
	s_nop 0
	global_load_dword v124, v[126:127], off
	ds_bpermute_b32 v105, v41, v68
	ds_bpermute_b32 v91, v40, v67
	ds_bpermute_b32 v72, v39, v5
	ds_bpermute_b32 v88, v44, v88
	ds_bpermute_b32 v70, v44, v70
	s_waitcnt lgkmcnt(4)
	v_add_f32_e32 v68, v68, v105
	ds_bpermute_b32 v105, v40, v68
	s_waitcnt lgkmcnt(4)
	v_add_f32_e32 v67, v67, v91
	s_waitcnt vmcnt(3)
	ds_bpermute_b32 v117, v36, v106
	ds_bpermute_b32 v91, v39, v67
	s_waitcnt lgkmcnt(5)
	v_add_f32_e32 v5, v5, v72
	s_waitcnt lgkmcnt(2)
	v_add_f32_e32 v68, v68, v105
	ds_bpermute_b32 v72, v44, v5
	s_waitcnt lgkmcnt(2)
	v_add_f32_e32 v105, v106, v117
	ds_bpermute_b32 v106, v37, v105
	s_waitcnt lgkmcnt(2)
	v_add_f32_e32 v5, v67, v91
	ds_bpermute_b32 v67, v41, v29
	ds_bpermute_b32 v91, v44, v5
	ds_bpermute_b32 v117, v39, v68
	s_waitcnt lgkmcnt(3)
	v_add_f32_e32 v5, v105, v106
	ds_bpermute_b32 v105, v38, v5
	s_waitcnt lgkmcnt(3)
	v_add_f32_e32 v29, v29, v67
	ds_bpermute_b32 v67, v40, v29
	s_waitcnt lgkmcnt(2)
	v_add_f32_e32 v68, v68, v117
	s_waitcnt lgkmcnt(1)
	v_add_f32_e32 v5, v5, v105
	ds_bpermute_b32 v106, v39, v5
	s_waitcnt lgkmcnt(1)
	v_add_f32_e32 v29, v29, v67
	ds_bpermute_b32 v67, v39, v29
	ds_bpermute_b32 v105, v44, v68
	ds_bpermute_b32 v68, v41, v27
	s_waitcnt lgkmcnt(3)
	v_add_f32_e32 v5, v5, v106
	s_waitcnt lgkmcnt(2)
	v_add_f32_e32 v29, v29, v67
	ds_bpermute_b32 v67, v40, v5
	s_waitcnt lgkmcnt(1)
	v_add_f32_e32 v27, v27, v68
	ds_bpermute_b32 v68, v40, v27
	ds_bpermute_b32 v106, v44, v29
	ds_bpermute_b32 v29, v41, v9
	s_waitcnt lgkmcnt(3)
	v_add_f32_e32 v5, v5, v67
	ds_bpermute_b32 v67, v41, v5
	s_waitcnt lgkmcnt(3)
	v_add_f32_e32 v27, v27, v68
	ds_bpermute_b32 v68, v39, v27
	s_waitcnt lgkmcnt(2)
	v_add_f32_e32 v9, v9, v29
	ds_bpermute_b32 v29, v40, v9
	s_waitcnt lgkmcnt(2)
	v_add_f32_e32 v5, v5, v67
	v_fmamk_f32 v5, v5, 0x39800000, v52
	v_mul_f32_e32 v67, 0x4f800000, v5
	v_cmp_gt_f32_e32 vcc, s85, v5
	s_waitcnt lgkmcnt(1)
	v_add_f32_e32 v27, v27, v68
	s_waitcnt lgkmcnt(0)
	v_add_f32_e32 v9, v9, v29
	v_cndmask_b32_e32 v5, v5, v67, vcc
	v_sqrt_f32_e32 v67, v5
	ds_bpermute_b32 v29, v39, v9
	v_add_u32_e32 v68, -1, v67
	v_fma_f32 v117, -v68, v67, v5
	v_cmp_ge_f32_e64 s[28:29], 0, v117
	v_add_u32_e32 v117, 1, v67
	s_waitcnt lgkmcnt(0)
	v_add_f32_e32 v9, v9, v29
	v_cndmask_b32_e64 v68, v67, v68, s[28:29]
	v_fma_f32 v67, -v117, v67, v5
	v_cmp_lt_f32_e64 s[28:29], 0, v67
	ds_bpermute_b32 v118, v44, v9
	s_nop 0
	v_cndmask_b32_e64 v67, v68, v117, s[28:29]
	v_mul_f32_e32 v68, 0x37800000, v67
	v_cndmask_b32_e32 v67, v67, v68, vcc
	v_cmp_class_f32_e32 vcc, v5, v53
	ds_bpermute_b32 v117, v44, v27
	s_nop 0
	v_cndmask_b32_e32 v5, v67, v5, vcc
	v_div_scale_f32 v67, s[28:29], v5, v5, 1.0
	v_rcp_f32_e32 v68, v67
	s_nop 0
	v_fma_f32 v9, -v67, v68, 1.0
	v_fmac_f32_e32 v68, v9, v68
	v_div_scale_f32 v9, vcc, 1.0, v5, 1.0
	v_mul_f32_e32 v27, v9, v68
	v_fma_f32 v29, -v67, v27, v9
	v_fmac_f32_e32 v27, v29, v68
	v_fma_f32 v9, -v67, v27, v9
	v_div_fmas_f32 v9, v9, v68, v27
	v_div_fixup_f32 v125, v9, v5, 1.0
	s_waitcnt vmcnt(0)
	v_pk_mul_f32 v[32:33], v[32:33], v[124:125]
	s_nop 0
	v_mul_f32_e32 v32, v32, v33
	v_mul_f32_e32 v5, 0x3d372713, v32
	v_mul_f32_e32 v5, v32, v5
	v_fma_f32 v5, v32, v5, v32
	v_mul_f32_e32 v67, 0x3f4c422a, v5
	v_cmp_nlt_f32_e64 s[28:29], |v67|, s86
	s_and_saveexec_b64 s[34:35], s[28:29]
	s_xor_b64 s[28:29], exec, s[34:35]
	s_cbranch_execz .LBB0_1209
	v_add_f32_e64 v5, |v67|, |v67|
	v_mul_f32_e32 v9, 0x3fb8aa3b, v5
	v_rndne_f32_e32 v27, v9
	v_sub_f32_e32 v29, v9, v27
	v_fma_f32 v9, v5, s87, -v9
	v_fmac_f32_e32 v9, 0x32a5705f, v5
	v_add_f32_e32 v9, v29, v9
	v_cvt_i32_f32_e32 v27, v27
	v_exp_f32_e32 v9, v9
	v_cmp_ngt_f32_e32 vcc, s88, v5
	v_ldexp_f32 v9, v9, v27
	s_nop 0
	v_cndmask_b32_e32 v9, 0, v9, vcc
	v_cmp_nlt_f32_e32 vcc, s89, v5
	s_nop 1
	v_cndmask_b32_e32 v5, v56, v9, vcc
	v_add_f32_e32 v5, 1.0, v5
	v_rcp_f32_e32 v5, v5
	s_nop 0
	v_fma_f32 v68, v5, -2.0, 1.0

; #define LAS __attribute__((address_space(3)))
; __device__ __forceinline__ void peer_expert_phase(const Args& a, int layer, LAS unsigned char* lds, int G, int bid) {
;     ...
;         for (int sidx = 0; sidx < 32; ++sidx) { const int s = (sidx + srot) & 31; const unsigned char* pus = PU + s * 128;
; #pragma unroll
;             for (int i = 0; i < 4; ++i) {
;                 int tok = tb + i * NGW; tok = tok < NTOK ? tok : tb;
;                 const u32x4 xq = *(const LAS u32x4*)(X8 + i * 4096 + s * 128 + 16 * l7);
;                 u32x4 r[16];
; #pragma unroll
;                 for (int c = 0; c < 16; ++c) { const unsigned eo = (unsigned)__shfl((int)(c < 8 ? eoa[i] : eob[i]), (8 * c + g8) & 63); r[c] = *(const u32x4*)(pus + (eo + lo16)); }
; #pragma unroll
;                 for (int c = 0; c < 16; ++c) { int d = pacc[i][c];
; #pragma unroll
;                     for (int q = 0; q < 4; ++q) d = __builtin_amdgcn_sdot4((int)r[c][q], (int)xq[q], d, false);
;                     pacc[i][c] = d; }
;                 __builtin_amdgcn_sched_barrier(0);
.LBB0_2267:
	s_bitcmp0_b32 s40, 7
	s_cbranch_scc0 .Lubar1_skip
	s_barrier
.Lubar1_skip:
	s_add_i32 s60, s67, s40
	s_and_b32 s81, s60, 0xf80
	s_add_u32 s60, s62, s81
	s_addc_u32 s61, s63, 0
	v_add_u32_e32 v117, s81, v36
	global_load_dwordx4 v[118:121], v186, s[60:61]
	global_load_dwordx4 v[122:125], v187, s[60:61]
	global_load_dwordx4 v[126:129], v188, s[60:61]
	global_load_dwordx4 v[130:133], v189, s[60:61]
	global_load_dwordx4 v[134:137], v190, s[60:61]
	global_load_dwordx4 v[138:141], v191, s[60:61]
	global_load_dwordx4 v[142:145], v192, s[60:61]
	global_load_dwordx4 v[146:149], v193, s[60:61]
	global_load_dwordx4 v[150:153], v194, s[60:61]
	global_load_dwordx4 v[158:161], v195, s[60:61]
	global_load_dwordx4 v[166:169], v196, s[60:61]
	global_load_dwordx4 v[154:157], v197, s[60:61]
	global_load_dwordx4 v[174:177], v198, s[60:61]
	global_load_dwordx4 v[162:165], v199, s[60:61]
	global_load_dwordx4 v[170:173], v200, s[60:61]
	global_load_dwordx4 v[178:181], v201, s[60:61]
	ds_read_b128 v[182:185], v117
	s_waitcnt lgkmcnt(0)
	s_waitcnt vmcnt(15)
	v_dot4c_i32_i8_e32 v116, v118, v182
	s_waitcnt vmcnt(14)
	v_dot4c_i32_i8_e32 v115, v122, v182
	v_dot4c_i32_i8_e32 v116, v119, v183
	s_waitcnt vmcnt(13)
	v_dot4c_i32_i8_e32 v27, v126, v182
	s_waitcnt vmcnt(12)
	v_dot4c_i32_i8_e32 v114, v130, v182
	v_dot4c_i32_i8_e32 v115, v123, v183
	v_dot4c_i32_i8_e32 v27, v127, v183
	v_dot4c_i32_i8_e32 v114, v131, v183
	s_waitcnt vmcnt(11)
	v_dot4c_i32_i8_e32 v113, v134, v182
	s_waitcnt vmcnt(10)
	v_dot4c_i32_i8_e32 v112, v138, v182
	v_dot4c_i32_i8_e32 v113, v135, v183
	v_dot4c_i32_i8_e32 v112, v139, v183
	v_dot4c_i32_i8_e32 v116, v120, v184
	s_waitcnt vmcnt(9)
	v_dot4c_i32_i8_e32 v111, v142, v182
	s_waitcnt vmcnt(8)
	v_dot4c_i32_i8_e32 v110, v146, v182
	v_dot4c_i32_i8_e32 v111, v143, v183
	v_dot4c_i32_i8_e32 v110, v147, v183
	s_waitcnt vmcnt(7)
	v_dot4c_i32_i8_e32 v109, v150, v182
	v_dot4c_i32_i8_e32 v109, v151, v183
	s_waitcnt vmcnt(6)
	v_dot4c_i32_i8_e32 v26, v158, v182
	v_dot4c_i32_i8_e32 v26, v159, v183
	v_dot4c_i32_i8_e32 v115, v124, v184
	v_dot4c_i32_i8_e32 v27, v128, v184
	v_dot4c_i32_i8_e32 v114, v132, v184
	s_waitcnt vmcnt(5)
	v_dot4c_i32_i8_e32 v106, v166, v182
	v_dot4c_i32_i8_e32 v106, v167, v183
	s_waitcnt vmcnt(4)
	v_dot4c_i32_i8_e32 v108, v154, v182
	v_dot4c_i32_i8_e32 v108, v155, v183
	v_dot4c_i32_i8_e32 v113, v136, v184
	s_waitcnt vmcnt(3)
	v_dot4c_i32_i8_e32 v104, v174, v182
	v_dot4c_i32_i8_e32 v104, v175, v183
	v_dot4c_i32_i8_e32 v112, v140, v184
	v_dot4c_i32_i8_e32 v111, v144, v184
	s_waitcnt vmcnt(2)
	v_dot4c_i32_i8_e32 v107, v162, v182
	v_dot4c_i32_i8_e32 v107, v163, v183
	v_dot4c_i32_i8_e32 v110, v148, v184
	v_dot4c_i32_i8_e32 v109, v152, v184
	v_dot4c_i32_i8_e32 v108, v156, v184
	v_dot4c_i32_i8_e32 v26, v160, v184
	v_dot4c_i32_i8_e32 v107, v164, v184
	s_waitcnt vmcnt(1)
	v_dot4c_i32_i8_e32 v105, v170, v182
	v_dot4c_i32_i8_e32 v105, v171, v183
	v_dot4c_i32_i8_e32 v106, v168, v184
	v_dot4c_i32_i8_e32 v105, v172, v184
	v_dot4c_i32_i8_e32 v104, v176, v184
	v_dot4c_i32_i8_e32 v116, v121, v185
	v_dot4c_i32_i8_e32 v115, v125, v185
	s_waitcnt vmcnt(0)
	v_dot4c_i32_i8_e32 v103, v178, v182
	v_dot4c_i32_i8_e32 v103, v179, v183
	v_dot4c_i32_i8_e32 v103, v180, v184
	v_dot4c_i32_i8_e32 v27, v129, v185
	v_dot4c_i32_i8_e32 v114, v133, v185
	v_dot4c_i32_i8_e32 v113, v137, v185
	v_dot4c_i32_i8_e32 v112, v141, v185
	v_dot4c_i32_i8_e32 v111, v145, v185
	v_dot4c_i32_i8_e32 v110, v149, v185
	v_dot4c_i32_i8_e32 v109, v153, v185
	v_dot4c_i32_i8_e32 v108, v157, v185
	v_dot4c_i32_i8_e32 v26, v161, v185
	v_dot4c_i32_i8_e32 v107, v165, v185
	v_dot4c_i32_i8_e32 v106, v169, v185
	v_dot4c_i32_i8_e32 v105, v173, v185
	v_dot4c_i32_i8_e32 v104, v177, v185
	v_dot4c_i32_i8_e32 v103, v181, v185
	global_load_dwordx4 v[118:121], v202, s[60:61]
	global_load_dwordx4 v[122:125], v203, s[60:61]
	global_load_dwordx4 v[126:129], v204, s[60:61]
	global_load_dwordx4 v[130:133], v205, s[60:61]
	global_load_dwordx4 v[134:137], v206, s[60:61]
	global_load_dwordx4 v[138:141], v207, s[60:61]
	global_load_dwordx4 v[142:145], v208, s[60:61]
	global_load_dwordx4 v[146:149], v209, s[60:61]
	global_load_dwordx4 v[150:153], v210, s[60:61]
	global_load_dwordx4 v[154:157], v211, s[60:61]
	global_load_dwordx4 v[158:161], v212, s[60:61]
	global_load_dwordx4 v[162:165], v213, s[60:61]
	global_load_dwordx4 v[166:169], v214, s[60:61]
	global_load_dwordx4 v[170:173], v215, s[60:61]
	global_load_dwordx4 v[174:177], v216, s[60:61]
	global_load_dwordx4 v[178:181], v217, s[60:61]
	ds_read_b128 v[182:185], v117 offset:4096
	s_waitcnt lgkmcnt(0)
	s_waitcnt vmcnt(15)
	v_dot4c_i32_i8_e32 v102, v118, v182
	s_waitcnt vmcnt(14)
	v_dot4c_i32_i8_e32 v101, v122, v182
	s_waitcnt vmcnt(13)
	v_dot4c_i32_i8_e32 v100, v126, v182
	s_waitcnt vmcnt(12)
	v_dot4c_i32_i8_e32 v99, v130, v182
	s_waitcnt vmcnt(11)
	v_dot4c_i32_i8_e32 v98, v134, v182
	s_waitcnt vmcnt(10)
	v_dot4c_i32_i8_e32 v97, v138, v182
	s_waitcnt vmcnt(9)
	v_dot4c_i32_i8_e32 v96, v142, v182
	s_waitcnt vmcnt(8)
	v_dot4c_i32_i8_e32 v95, v146, v182
	s_waitcnt vmcnt(7)
	v_dot4c_i32_i8_e32 v94, v150, v182
	s_waitcnt vmcnt(6)
	v_dot4c_i32_i8_e32 v93, v154, v182
	s_waitcnt vmcnt(5)
; #define LAS __attribute__((address_space(3)))
; __device__ __forceinline__ void peer_expert_phase(const Args& a, int layer, LAS unsigned char* lds, int G, int bid) {
;     ...
;             for (int i = 0; i < 4; ++i) {
;                 int tok = tb + i * NGW; tok = tok < NTOK ? tok : tb;
;                 const u32x4 xq = *(const LAS u32x4*)(X8 + i * 4096 + s * 128 + 16 * l7);
;                 u32x4 r[16];
; #pragma unroll
;                 for (int c = 0; c < 16; ++c) { const unsigned eo = (unsigned)__shfl((int)(c < 8 ? eoa[i] : eob[i]), (8 * c + g8) & 63); r[c] = *(const u32x4*)(pus + (eo + lo16)); }
; #pragma unroll
;                 for (int c = 0; c < 16; ++c) { int d = pacc[i][c];
; #pragma unroll
;                     for (int q = 0; q < 4; ++q) d = __builtin_amdgcn_sdot4((int)r[c][q], (int)xq[q], d, false);
;                     pacc[i][c] = d; }
;                 __builtin_amdgcn_sched_barrier(0);
	v_dot4c_i32_i8_e32 v92, v158, v182
	v_dot4c_i32_i8_e32 v102, v119, v183
	v_dot4c_i32_i8_e32 v101, v123, v183
	v_dot4c_i32_i8_e32 v100, v127, v183
	v_dot4c_i32_i8_e32 v99, v131, v183
	v_dot4c_i32_i8_e32 v98, v135, v183
	v_dot4c_i32_i8_e32 v97, v139, v183
	v_dot4c_i32_i8_e32 v96, v143, v183
	v_dot4c_i32_i8_e32 v95, v147, v183
	v_dot4c_i32_i8_e32 v94, v151, v183
	v_dot4c_i32_i8_e32 v93, v155, v183
	v_dot4c_i32_i8_e32 v92, v159, v183
	v_dot4c_i32_i8_e32 v102, v120, v184
	v_dot4c_i32_i8_e32 v101, v124, v184
	v_dot4c_i32_i8_e32 v100, v128, v184
	v_dot4c_i32_i8_e32 v99, v132, v184
	v_dot4c_i32_i8_e32 v98, v136, v184
	v_dot4c_i32_i8_e32 v97, v140, v184
	v_dot4c_i32_i8_e32 v96, v144, v184
	v_dot4c_i32_i8_e32 v95, v148, v184
	v_dot4c_i32_i8_e32 v94, v152, v184
	v_dot4c_i32_i8_e32 v93, v156, v184
	v_dot4c_i32_i8_e32 v92, v160, v184
	v_dot4c_i32_i8_e32 v102, v121, v185
	v_dot4c_i32_i8_e32 v101, v125, v185
	v_dot4c_i32_i8_e32 v100, v129, v185
	v_dot4c_i32_i8_e32 v99, v133, v185
	v_dot4c_i32_i8_e32 v98, v137, v185
	v_dot4c_i32_i8_e32 v97, v141, v185
	v_dot4c_i32_i8_e32 v96, v145, v185
	v_dot4c_i32_i8_e32 v95, v149, v185
	v_dot4c_i32_i8_e32 v94, v153, v185
	v_dot4c_i32_i8_e32 v93, v157, v185
	v_dot4c_i32_i8_e32 v92, v161, v185
	s_waitcnt vmcnt(4)
	v_dot4c_i32_i8_e32 v89, v162, v182
	v_dot4c_i32_i8_e32 v89, v163, v183
	s_waitcnt vmcnt(3)
	v_dot4c_i32_i8_e32 v91, v166, v182
	v_dot4c_i32_i8_e32 v91, v167, v183
	s_waitcnt vmcnt(2)
	v_dot4c_i32_i8_e32 v90, v170, v182
	v_dot4c_i32_i8_e32 v90, v171, v183
	s_waitcnt vmcnt(1)
	v_dot4c_i32_i8_e32 v88, v174, v182
	v_dot4c_i32_i8_e32 v88, v175, v183
	s_waitcnt vmcnt(0)
	v_dot4c_i32_i8_e32 v87, v178, v182
	v_dot4c_i32_i8_e32 v87, v179, v183
	v_dot4c_i32_i8_e32 v89, v164, v184
	v_dot4c_i32_i8_e32 v91, v168, v184
	v_dot4c_i32_i8_e32 v90, v172, v184
	v_dot4c_i32_i8_e32 v88, v176, v184
	v_dot4c_i32_i8_e32 v87, v180, v184
	v_dot4c_i32_i8_e32 v89, v165, v185
	v_dot4c_i32_i8_e32 v91, v169, v185
	v_dot4c_i32_i8_e32 v90, v173, v185
	v_dot4c_i32_i8_e32 v88, v177, v185
	v_dot4c_i32_i8_e32 v87, v181, v185
	global_load_dwordx4 v[118:121], v218, s[60:61]
	global_load_dwordx4 v[122:125], v219, s[60:61]
	global_load_dwordx4 v[126:129], v220, s[60:61]
	global_load_dwordx4 v[130:133], v221, s[60:61]
	global_load_dwordx4 v[134:137], v222, s[60:61]
	global_load_dwordx4 v[138:141], v223, s[60:61]
	global_load_dwordx4 v[142:145], v224, s[60:61]
	global_load_dwordx4 v[146:149], v225, s[60:61]
	global_load_dwordx4 v[150:153], v226, s[60:61]
	global_load_dwordx4 v[154:157], v227, s[60:61]
	global_load_dwordx4 v[158:161], v229, s[60:61]
	global_load_dwordx4 v[162:165], v230, s[60:61]
	global_load_dwordx4 v[166:169], v231, s[60:61]
	global_load_dwordx4 v[170:173], v232, s[60:61]
	global_load_dwordx4 v[174:177], v233, s[60:61]
	global_load_dwordx4 v[178:181], v234, s[60:61]
	ds_read_b128 v[182:185], v117 offset:8192
	s_waitcnt lgkmcnt(0)
	s_waitcnt vmcnt(15)
	v_dot4c_i32_i8_e32 v86, v118, v182
	s_waitcnt vmcnt(14)
	v_dot4c_i32_i8_e32 v85, v122, v182
	s_waitcnt vmcnt(13)
	v_dot4c_i32_i8_e32 v84, v126, v182
	s_waitcnt vmcnt(12)
	v_dot4c_i32_i8_e32 v83, v130, v182
	s_waitcnt vmcnt(11)
	v_dot4c_i32_i8_e32 v82, v134, v182
	s_waitcnt vmcnt(10)
	v_dot4c_i32_i8_e32 v81, v138, v182
	s_waitcnt vmcnt(9)
	v_dot4c_i32_i8_e32 v80, v142, v182
	s_waitcnt vmcnt(8)
	v_dot4c_i32_i8_e32 v79, v146, v182
	s_waitcnt vmcnt(7)
	v_dot4c_i32_i8_e32 v78, v150, v182
	s_waitcnt vmcnt(6)
	v_dot4c_i32_i8_e32 v77, v154, v182
	s_waitcnt vmcnt(5)
	v_dot4c_i32_i8_e32 v76, v158, v182
	v_dot4c_i32_i8_e32 v86, v119, v183
	v_dot4c_i32_i8_e32 v85, v123, v183
	v_dot4c_i32_i8_e32 v84, v127, v183
	v_dot4c_i32_i8_e32 v83, v131, v183
	v_dot4c_i32_i8_e32 v82, v135, v183
	v_dot4c_i32_i8_e32 v81, v139, v183
	v_dot4c_i32_i8_e32 v80, v143, v183
	v_dot4c_i32_i8_e32 v79, v147, v183
	v_dot4c_i32_i8_e32 v78, v151, v183
	v_dot4c_i32_i8_e32 v77, v155, v183
	v_dot4c_i32_i8_e32 v76, v159, v183
	v_dot4c_i32_i8_e32 v86, v120, v184
	v_dot4c_i32_i8_e32 v85, v124, v184
	v_dot4c_i32_i8_e32 v84, v128, v184
	v_dot4c_i32_i8_e32 v83, v132, v184
	v_dot4c_i32_i8_e32 v82, v136, v184
	v_dot4c_i32_i8_e32 v81, v140, v184
	v_dot4c_i32_i8_e32 v80, v144, v184
	v_dot4c_i32_i8_e32 v79, v148, v184
	v_dot4c_i32_i8_e32 v78, v152, v184
	v_dot4c_i32_i8_e32 v77, v156, v184
	v_dot4c_i32_i8_e32 v76, v160, v184
	v_dot4c_i32_i8_e32 v86, v121, v185
	v_dot4c_i32_i8_e32 v85, v125, v185
	v_dot4c_i32_i8_e32 v84, v129, v185
	v_dot4c_i32_i8_e32 v83, v133, v185
	v_dot4c_i32_i8_e32 v82, v137, v185
	v_dot4c_i32_i8_e32 v81, v141, v185
	v_dot4c_i32_i8_e32 v80, v145, v185
	v_dot4c_i32_i8_e32 v79, v149, v185
	v_dot4c_i32_i8_e32 v78, v153, v185
	v_dot4c_i32_i8_e32 v77, v157, v185
	v_dot4c_i32_i8_e32 v76, v161, v185
	s_waitcnt vmcnt(4)
	v_dot4c_i32_i8_e32 v75, v162, v182
	v_dot4c_i32_i8_e32 v75, v163, v183
	s_waitcnt vmcnt(3)
	v_dot4c_i32_i8_e32 v74, v166, v182
	v_dot4c_i32_i8_e32 v74, v167, v183
	s_waitcnt vmcnt(2)
	v_dot4c_i32_i8_e32 v73, v170, v182
	v_dot4c_i32_i8_e32 v73, v171, v183
	s_waitcnt vmcnt(1)
	v_dot4c_i32_i8_e32 v72, v174, v182
	v_dot4c_i32_i8_e32 v72, v175, v183
	s_waitcnt vmcnt(0)
; #define LAS __attribute__((address_space(3)))
; __device__ __forceinline__ void peer_expert_phase(const Args& a, int layer, LAS unsigned char* lds, int G, int bid) {
;     ...
;             for (int i = 0; i < 4; ++i) {
;                 int tok = tb + i * NGW; tok = tok < NTOK ? tok : tb;
;                 const u32x4 xq = *(const LAS u32x4*)(X8 + i * 4096 + s * 128 + 16 * l7);
;                 u32x4 r[16];
; #pragma unroll
;                 for (int c = 0; c < 16; ++c) { const unsigned eo = (unsigned)__shfl((int)(c < 8 ? eoa[i] : eob[i]), (8 * c + g8) & 63); r[c] = *(const u32x4*)(pus + (eo + lo16)); }
; #pragma unroll
;                 for (int c = 0; c < 16; ++c) { int d = pacc[i][c];
; #pragma unroll
;                     for (int q = 0; q < 4; ++q) d = __builtin_amdgcn_sdot4((int)r[c][q], (int)xq[q], d, false);
;                     pacc[i][c] = d; }
;                 __builtin_amdgcn_sched_barrier(0);
;             }
;         }
;         float pa[4], pb[4];
; #pragma unroll
;         for (int i = 0; i < 4; ++i) { pa[i] = 0.f; pb[i] = 0.f;
; #pragma unroll
;             for (int c = 0; c < 16; ++c) { float v = (float)pacc[i][c]; v += __shfl_xor(v, 1); v += __shfl_xor(v, 2); v += __shfl_xor(v, 4);
;                 const float t = __shfl(v, 8 * (lane & 7));
;                 if (c < 8) pa[i] = (g8 == c) ? t : pa[i]; else pb[i] = (g8 == c - 8) ? t : pb[i]; } }
	v_dot4c_i32_i8_e32 v71, v178, v182
	v_dot4c_i32_i8_e32 v71, v179, v183
	v_dot4c_i32_i8_e32 v75, v164, v184
	v_dot4c_i32_i8_e32 v74, v168, v184
	v_dot4c_i32_i8_e32 v73, v172, v184
	v_dot4c_i32_i8_e32 v72, v176, v184
	v_dot4c_i32_i8_e32 v71, v180, v184
	v_dot4c_i32_i8_e32 v75, v165, v185
	v_dot4c_i32_i8_e32 v74, v169, v185
	v_dot4c_i32_i8_e32 v73, v173, v185
	v_dot4c_i32_i8_e32 v72, v177, v185
	v_dot4c_i32_i8_e32 v71, v181, v185
	global_load_dwordx4 v[118:121], v235, s[60:61]
	global_load_dwordx4 v[122:125], v236, s[60:61]
	global_load_dwordx4 v[126:129], v237, s[60:61]
	global_load_dwordx4 v[130:133], v238, s[60:61]
	global_load_dwordx4 v[134:137], v239, s[60:61]
	global_load_dwordx4 v[138:141], v240, s[60:61]
	global_load_dwordx4 v[142:145], v241, s[60:61]
	global_load_dwordx4 v[146:149], v242, s[60:61]
	global_load_dwordx4 v[150:153], v243, s[60:61]
	global_load_dwordx4 v[154:157], v244, s[60:61]
	global_load_dwordx4 v[158:161], v245, s[60:61]
	global_load_dwordx4 v[162:165], v246, s[60:61]
	global_load_dwordx4 v[166:169], v247, s[60:61]
	global_load_dwordx4 v[170:173], v248, s[60:61]
	global_load_dwordx4 v[174:177], v249, s[60:61]
	global_load_dwordx4 v[178:181], v250, s[60:61]
	ds_read_b128 v[182:185], v117 offset:12288
	s_waitcnt lgkmcnt(0)
	s_waitcnt vmcnt(15)
	v_dot4c_i32_i8_e32 v70, v118, v182
	s_waitcnt vmcnt(14)
	v_dot4c_i32_i8_e32 v69, v122, v182
	s_waitcnt vmcnt(13)
	v_dot4c_i32_i8_e32 v68, v126, v182
	s_waitcnt vmcnt(12)
	v_dot4c_i32_i8_e32 v67, v130, v182
	s_waitcnt vmcnt(11)
	v_dot4c_i32_i8_e32 v66, v134, v182
	s_waitcnt vmcnt(10)
	v_dot4c_i32_i8_e32 v65, v138, v182
	s_waitcnt vmcnt(9)
	v_dot4c_i32_i8_e32 v64, v142, v182
	s_waitcnt vmcnt(8)
	v_dot4c_i32_i8_e32 v63, v146, v182
	s_waitcnt vmcnt(7)
	v_dot4c_i32_i8_e32 v62, v150, v182
	s_waitcnt vmcnt(6)
	v_dot4c_i32_i8_e32 v61, v154, v182
	s_waitcnt vmcnt(5)
	v_dot4c_i32_i8_e32 v60, v158, v182
	v_dot4c_i32_i8_e32 v70, v119, v183
	v_dot4c_i32_i8_e32 v69, v123, v183
	v_dot4c_i32_i8_e32 v68, v127, v183
	v_dot4c_i32_i8_e32 v67, v131, v183
	v_dot4c_i32_i8_e32 v66, v135, v183
	v_dot4c_i32_i8_e32 v65, v139, v183
	v_dot4c_i32_i8_e32 v64, v143, v183
	v_dot4c_i32_i8_e32 v63, v147, v183
	v_dot4c_i32_i8_e32 v62, v151, v183
	v_dot4c_i32_i8_e32 v61, v155, v183
	v_dot4c_i32_i8_e32 v60, v159, v183
	v_dot4c_i32_i8_e32 v70, v120, v184
	v_dot4c_i32_i8_e32 v69, v124, v184
	v_dot4c_i32_i8_e32 v68, v128, v184
	v_dot4c_i32_i8_e32 v67, v132, v184
	v_dot4c_i32_i8_e32 v66, v136, v184
	v_dot4c_i32_i8_e32 v65, v140, v184
	v_dot4c_i32_i8_e32 v64, v144, v184
	v_dot4c_i32_i8_e32 v63, v148, v184
	v_dot4c_i32_i8_e32 v62, v152, v184
	v_dot4c_i32_i8_e32 v61, v156, v184
	v_dot4c_i32_i8_e32 v60, v160, v184
	v_dot4c_i32_i8_e32 v70, v121, v185
	v_dot4c_i32_i8_e32 v69, v125, v185
	v_dot4c_i32_i8_e32 v68, v129, v185
	v_dot4c_i32_i8_e32 v67, v133, v185
	v_dot4c_i32_i8_e32 v66, v137, v185
	v_dot4c_i32_i8_e32 v65, v141, v185
	v_dot4c_i32_i8_e32 v64, v145, v185
	v_dot4c_i32_i8_e32 v63, v149, v185
	v_dot4c_i32_i8_e32 v62, v153, v185
	v_dot4c_i32_i8_e32 v61, v157, v185
	v_dot4c_i32_i8_e32 v60, v161, v185
	s_waitcnt vmcnt(4)
	v_dot4c_i32_i8_e32 v59, v162, v182
	v_dot4c_i32_i8_e32 v59, v163, v183
	s_waitcnt vmcnt(3)
	v_dot4c_i32_i8_e32 v19, v166, v182
	v_dot4c_i32_i8_e32 v19, v167, v183
	s_waitcnt vmcnt(2)
	v_dot4c_i32_i8_e32 v23, v170, v182
	v_dot4c_i32_i8_e32 v23, v171, v183
	s_waitcnt vmcnt(1)
	v_dot4c_i32_i8_e32 v21, v174, v182
	v_dot4c_i32_i8_e32 v21, v175, v183
	s_waitcnt vmcnt(0)
	v_dot4c_i32_i8_e32 v7, v178, v182
	v_dot4c_i32_i8_e32 v7, v179, v183
	v_dot4c_i32_i8_e32 v59, v164, v184
	v_dot4c_i32_i8_e32 v19, v168, v184
	v_dot4c_i32_i8_e32 v23, v172, v184
	v_dot4c_i32_i8_e32 v21, v176, v184
	v_dot4c_i32_i8_e32 v7, v180, v184
	v_dot4c_i32_i8_e32 v59, v165, v185
	v_dot4c_i32_i8_e32 v19, v169, v185
	v_dot4c_i32_i8_e32 v23, v173, v185
	v_dot4c_i32_i8_e32 v21, v177, v185
	v_dot4c_i32_i8_e32 v7, v181, v185
	s_addk_i32 s40, 0x80
	s_cmpk_eq_i32 s40, 0x1000
	s_cbranch_scc0 .LBB0_2267
	v_cvt_f32_i32_e32 v116, v116
	v_cvt_f32_i32_e32 v115, v115
	v_cvt_f32_i32_e32 v119, v27
	v_mul_f32_e32 v27, 0x3c010204, v3
	ds_bpermute_b32 v117, v34, v116
	ds_bpermute_b32 v118, v34, v115
	v_cvt_f32_i32_e32 v3, v114
	ds_bpermute_b32 v114, v34, v119
	v_cvt_f32_i32_e32 v112, v112
	s_waitcnt lgkmcnt(2)
	v_add_f32_e32 v116, v116, v117
	s_waitcnt lgkmcnt(1)
	v_add_f32_e32 v115, v115, v118
	ds_bpermute_b32 v117, v33, v116
	ds_bpermute_b32 v118, v33, v115
	ds_bpermute_b32 v120, v34, v3
	s_waitcnt lgkmcnt(3)
	v_add_f32_e32 v114, v119, v114
	ds_bpermute_b32 v119, v33, v114
	s_waitcnt lgkmcnt(3)
	v_add_f32_e32 v116, v116, v117
	s_waitcnt lgkmcnt(2)
	v_add_f32_e32 v115, v115, v118
	ds_bpermute_b32 v117, v32, v116
	ds_bpermute_b32 v118, v32, v115
	s_waitcnt lgkmcnt(3)
	v_add_f32_e32 v3, v3, v120
	s_waitcnt lgkmcnt(2)
	v_add_f32_e32 v114, v114, v119
	v_cvt_f32_i32_e32 v113, v113
	s_waitcnt lgkmcnt(1)
	v_add_f32_e32 v116, v116, v117
	s_waitcnt lgkmcnt(0)
	v_add_f32_e32 v115, v115, v118
	ds_bpermute_b32 v116, v37, v116
	ds_bpermute_b32 v118, v33, v3
	ds_bpermute_b32 v115, v37, v115
	ds_bpermute_b32 v117, v32, v114
	ds_bpermute_b32 v119, v34, v113
	s_waitcnt lgkmcnt(4)
	v_cndmask_b32_e64 v116, 0, v116, s[6:7]
	s_waitcnt lgkmcnt(3)
	v_add_f32_e32 v3, v3, v118
	s_waitcnt lgkmcnt(2)
	v_cndmask_b32_e64 v115, v116, v115, s[8:9]
	ds_bpermute_b32 v116, v32, v3
	s_waitcnt lgkmcnt(2)
	v_add_f32_e32 v114, v114, v117
	ds_bpermute_b32 v114, v37, v114
	s_waitcnt lgkmcnt(2)
	v_add_f32_e32 v113, v113, v119
	ds_bpermute_b32 v117, v33, v113
	s_waitcnt lgkmcnt(2)
	v_add_f32_e32 v3, v3, v116
	ds_bpermute_b32 v116, v34, v112
	ds_bpermute_b32 v3, v37, v3
	s_waitcnt lgkmcnt(3)
; __device__ __forceinline__ void peer_expert_phase(const Args& a, int layer, LAS unsigned char* lds, int G, int bid) {
;     ...
;         float pa[4], pb[4];
; #pragma unroll
;         for (int i = 0; i < 4; ++i) { pa[i] = 0.f; pb[i] = 0.f;
; #pragma unroll
;             for (int c = 0; c < 16; ++c) { float v = (float)pacc[i][c]; v += __shfl_xor(v, 1); v += __shfl_xor(v, 2); v += __shfl_xor(v, 4);
;                 const float t = __shfl(v, 8 * (lane & 7));
;                 if (c < 8) pa[i] = (g8 == c) ? t : pa[i]; else pb[i] = (g8 == c - 8) ? t : pb[i]; } }
	v_cndmask_b32_e64 v114, v115, v114, s[10:11]
	v_cvt_f32_i32_e32 v110, v110
	s_waitcnt lgkmcnt(2)
	v_add_f32_e32 v113, v113, v117
	s_waitcnt lgkmcnt(1)
	v_add_f32_e32 v112, v112, v116
	ds_bpermute_b32 v116, v33, v112
	s_waitcnt lgkmcnt(1)
	v_cndmask_b32_e64 v3, v114, v3, s[12:13]
	v_cvt_f32_i32_e32 v111, v111
	ds_bpermute_b32 v117, v32, v113
	v_cvt_f32_i32_e32 v109, v109
	s_waitcnt lgkmcnt(1)
	v_add_f32_e32 v112, v112, v116
	ds_bpermute_b32 v114, v32, v112
	ds_bpermute_b32 v115, v34, v111
	s_waitcnt lgkmcnt(2)
	v_add_f32_e32 v113, v113, v117
	ds_bpermute_b32 v113, v37, v113
	v_cvt_f32_i32_e32 v108, v108
	s_waitcnt lgkmcnt(2)
	v_add_f32_e32 v112, v112, v114
	ds_bpermute_b32 v114, v34, v110
	ds_bpermute_b32 v112, v37, v112
	s_waitcnt lgkmcnt(3)
	v_add_f32_e32 v111, v111, v115
	ds_bpermute_b32 v115, v33, v111
	s_waitcnt lgkmcnt(3)
	v_cndmask_b32_e64 v3, v3, v113, s[14:15]
	s_waitcnt lgkmcnt(2)
	v_add_f32_e32 v110, v110, v114
	ds_bpermute_b32 v114, v33, v110
	ds_bpermute_b32 v113, v34, v109
	s_waitcnt lgkmcnt(3)
	v_cndmask_b32_e64 v3, v3, v112, s[16:17]
	s_waitcnt lgkmcnt(2)
	v_add_f32_e32 v111, v111, v115
	ds_bpermute_b32 v115, v32, v111
	s_waitcnt lgkmcnt(2)
	v_add_f32_e32 v110, v110, v114
	ds_bpermute_b32 v112, v32, v110
	s_waitcnt lgkmcnt(2)
	v_add_f32_e32 v109, v109, v113
	ds_bpermute_b32 v113, v33, v109
	s_waitcnt lgkmcnt(2)
	v_add_f32_e32 v111, v111, v115
	ds_bpermute_b32 v111, v37, v111
	s_waitcnt lgkmcnt(2)
	v_add_f32_e32 v110, v110, v112
	ds_bpermute_b32 v112, v34, v108
	v_cvt_f32_i32_e32 v114, v26
	s_waitcnt lgkmcnt(2)
	v_add_f32_e32 v109, v109, v113
	ds_bpermute_b32 v110, v37, v110
	ds_bpermute_b32 v113, v32, v109
	s_waitcnt lgkmcnt(2)
	v_add_f32_e32 v108, v108, v112
	ds_bpermute_b32 v112, v33, v108
	v_cndmask_b32_e64 v3, v3, v111, s[18:19]
	ds_bpermute_b32 v111, v34, v114
	s_waitcnt lgkmcnt(3)
	v_cndmask_b32_e64 v26, v3, v110, s[20:21]
	s_waitcnt lgkmcnt(2)
	v_add_f32_e32 v3, v109, v113
	s_waitcnt lgkmcnt(1)
	v_add_f32_e32 v108, v108, v112
	ds_bpermute_b32 v109, v32, v108
	s_waitcnt lgkmcnt(1)
	v_add_f32_e32 v110, v114, v111
	ds_bpermute_b32 v111, v33, v110
	v_cvt_f32_i32_e32 v112, v107
	ds_bpermute_b32 v107, v37, v3
	s_waitcnt lgkmcnt(2)
	v_add_f32_e32 v3, v108, v109
	v_cvt_f32_i32_e32 v108, v106
	ds_bpermute_b32 v109, v34, v112
	s_waitcnt lgkmcnt(2)
	v_add_f32_e32 v110, v110, v111
	ds_bpermute_b32 v111, v32, v110
	ds_bpermute_b32 v113, v34, v108
	ds_bpermute_b32 v106, v37, v3
	s_waitcnt lgkmcnt(3)
	v_add_f32_e32 v3, v112, v109
	ds_bpermute_b32 v109, v33, v3
	s_waitcnt lgkmcnt(3)
	v_add_f32_e32 v110, v110, v111
	s_waitcnt lgkmcnt(2)
	v_add_f32_e32 v111, v108, v113
	ds_bpermute_b32 v112, v33, v111
	v_cvt_f32_i32_e32 v105, v105
	s_waitcnt lgkmcnt(1)
	v_add_f32_e32 v3, v3, v109
	ds_bpermute_b32 v108, v37, v110
	ds_bpermute_b32 v109, v32, v3
	s_waitcnt lgkmcnt(2)
	v_add_f32_e32 v110, v111, v112
	ds_bpermute_b32 v113, v34, v105
	ds_bpermute_b32 v112, v32, v110
	v_cvt_f32_i32_e32 v104, v104
	s_waitcnt lgkmcnt(2)
	v_add_f32_e32 v3, v3, v109
	ds_bpermute_b32 v111, v37, v3
	s_waitcnt lgkmcnt(2)
	v_add_f32_e32 v105, v105, v113
	ds_bpermute_b32 v109, v34, v104
	s_waitcnt lgkmcnt(2)
	v_add_f32_e32 v3, v110, v112
	ds_bpermute_b32 v110, v33, v105
	v_cvt_f32_i32_e32 v103, v103
	ds_bpermute_b32 v115, v37, v3
	s_waitcnt lgkmcnt(2)
	v_add_f32_e32 v104, v104, v109
	ds_bpermute_b32 v109, v33, v104
	s_waitcnt lgkmcnt(2)
	v_add_f32_e32 v3, v105, v110
	ds_bpermute_b32 v105, v34, v103
	ds_bpermute_b32 v110, v32, v3
	v_cvt_f32_i32_e32 v102, v102
	s_waitcnt lgkmcnt(2)
	v_add_f32_e32 v104, v104, v109
	ds_bpermute_b32 v109, v32, v104
	s_waitcnt lgkmcnt(2)
	v_add_f32_e32 v103, v103, v105
	ds_bpermute_b32 v105, v33, v103
	s_waitcnt lgkmcnt(2)
	v_add_f32_e32 v3, v3, v110
	ds_bpermute_b32 v110, v34, v102
	ds_bpermute_b32 v116, v37, v3
	s_waitcnt lgkmcnt(3)
	v_add_f32_e32 v3, v104, v109
	s_waitcnt lgkmcnt(2)
	v_add_f32_e32 v103, v103, v105
	ds_bpermute_b32 v104, v32, v103
	s_waitcnt lgkmcnt(2)
	v_add_f32_e32 v102, v102, v110
	v_cvt_f32_i32_e32 v101, v101
	ds_bpermute_b32 v105, v33, v102
	v_cvt_f32_i32_e32 v100, v100
	ds_bpermute_b32 v117, v37, v3
	s_waitcnt lgkmcnt(2)
	v_add_f32_e32 v3, v103, v104
	ds_bpermute_b32 v103, v34, v101
	s_waitcnt lgkmcnt(2)
	v_add_f32_e32 v102, v102, v105
	ds_bpermute_b32 v105, v34, v100
	ds_bpermute_b32 v104, v32, v102
	ds_bpermute_b32 v118, v37, v3
	s_waitcnt lgkmcnt(3)
	v_add_f32_e32 v3, v101, v103
	ds_bpermute_b32 v101, v33, v3
	s_waitcnt lgkmcnt(3)
	v_add_f32_e32 v103, v100, v105
	s_waitcnt lgkmcnt(2)
	v_add_f32_e32 v102, v102, v104
	ds_bpermute_b32 v104, v33, v103
	v_cvt_f32_i32_e32 v99, v99
	s_waitcnt lgkmcnt(1)
	v_add_f32_e32 v3, v3, v101
	ds_bpermute_b32 v101, v32, v3
	ds_bpermute_b32 v100, v37, v102
	s_waitcnt lgkmcnt(2)
	v_add_f32_e32 v102, v103, v104
	v_cvt_f32_i32_e32 v103, v98
	ds_bpermute_b32 v105, v34, v99
	ds_bpermute_b32 v104, v32, v102
	s_waitcnt lgkmcnt(3)
	v_add_f32_e32 v3, v3, v101
	ds_bpermute_b32 v101, v34, v103
	ds_bpermute_b32 v98, v37, v3
	s_waitcnt lgkmcnt(3)
	v_add_f32_e32 v99, v99, v105
	s_waitcnt lgkmcnt(2)
	v_add_f32_e32 v3, v102, v104
	ds_bpermute_b32 v102, v33, v99
	s_waitcnt lgkmcnt(2)
	v_add_f32_e32 v101, v103, v101
	v_cvt_f32_i32_e32 v103, v97
	ds_bpermute_b32 v97, v37, v3
	ds_bpermute_b32 v104, v33, v101
	s_waitcnt lgkmcnt(2)
	v_add_f32_e32 v3, v99, v102
	ds_bpermute_b32 v99, v34, v103
	ds_bpermute_b32 v102, v32, v3
	v_cvt_f32_i32_e32 v105, v96
	s_waitcnt lgkmcnt(2)
	v_add_f32_e32 v101, v101, v104
	ds_bpermute_b32 v104, v32, v101
	s_waitcnt lgkmcnt(2)
	v_add_f32_e32 v99, v103, v99
	ds_bpermute_b32 v103, v33, v99
	s_waitcnt lgkmcnt(2)
	v_add_f32_e32 v3, v3, v102
	ds_bpermute_b32 v102, v34, v105
	ds_bpermute_b32 v96, v37, v3
	s_waitcnt lgkmcnt(3)
; __device__ __forceinline__ void peer_expert_phase(const Args& a, int layer, LAS unsigned char* lds, int G, int bid) {
;     ...
;         float pa[4], pb[4];
; #pragma unroll
;         for (int i = 0; i < 4; ++i) { pa[i] = 0.f; pb[i] = 0.f;
; #pragma unroll
;             for (int c = 0; c < 16; ++c) { float v = (float)pacc[i][c]; v += __shfl_xor(v, 1); v += __shfl_xor(v, 2); v += __shfl_xor(v, 4);
;                 const float t = __shfl(v, 8 * (lane & 7));
;                 if (c < 8) pa[i] = (g8 == c) ? t : pa[i]; else pb[i] = (g8 == c - 8) ? t : pb[i]; } }
	v_add_f32_e32 v3, v101, v104
	s_waitcnt lgkmcnt(2)
	v_add_f32_e32 v99, v99, v103
	ds_bpermute_b32 v101, v32, v99
	v_cvt_f32_i32_e32 v104, v95
	s_waitcnt lgkmcnt(2)
	v_add_f32_e32 v102, v105, v102
	ds_bpermute_b32 v103, v33, v102
	ds_bpermute_b32 v95, v37, v3
	s_waitcnt lgkmcnt(2)
	v_add_f32_e32 v3, v99, v101
	v_cvt_f32_i32_e32 v94, v94
	ds_bpermute_b32 v99, v34, v104
	s_waitcnt lgkmcnt(2)
	v_add_f32_e32 v101, v102, v103
	ds_bpermute_b32 v102, v32, v101
	ds_bpermute_b32 v105, v34, v94
	ds_bpermute_b32 v103, v37, v3
	s_waitcnt lgkmcnt(3)
	v_add_f32_e32 v3, v104, v99
	ds_bpermute_b32 v99, v33, v3
	s_waitcnt lgkmcnt(3)
	v_add_f32_e32 v101, v101, v102
	s_waitcnt lgkmcnt(2)
	v_add_f32_e32 v94, v94, v105
	ds_bpermute_b32 v102, v33, v94
	v_cvt_f32_i32_e32 v93, v93
	s_waitcnt lgkmcnt(1)
	v_add_f32_e32 v3, v3, v99
	ds_bpermute_b32 v99, v32, v3
	v_cvt_f32_i32_e32 v92, v92
	s_waitcnt lgkmcnt(1)
	v_add_f32_e32 v94, v94, v102
	ds_bpermute_b32 v102, v34, v93
	ds_bpermute_b32 v105, v37, v101
	ds_bpermute_b32 v101, v32, v94
	s_waitcnt lgkmcnt(3)
	v_add_f32_e32 v3, v3, v99
	ds_bpermute_b32 v99, v34, v92
	s_waitcnt lgkmcnt(3)
	v_add_f32_e32 v93, v93, v102
	ds_bpermute_b32 v109, v37, v3
	s_waitcnt lgkmcnt(2)
	v_add_f32_e32 v3, v94, v101
	ds_bpermute_b32 v94, v33, v93
	s_waitcnt lgkmcnt(2)
	v_add_f32_e32 v92, v92, v99
	v_cvt_f32_i32_e32 v99, v89
	ds_bpermute_b32 v101, v33, v92
	ds_bpermute_b32 v89, v37, v3
	s_waitcnt lgkmcnt(2)
	v_add_f32_e32 v3, v93, v94
	ds_bpermute_b32 v93, v34, v99
	ds_bpermute_b32 v94, v32, v3
	s_waitcnt lgkmcnt(3)
	v_add_f32_e32 v92, v92, v101
	v_cvt_f32_i32_e32 v102, v91
	ds_bpermute_b32 v101, v32, v92
	s_waitcnt lgkmcnt(2)
	v_add_f32_e32 v93, v99, v93
	ds_bpermute_b32 v99, v33, v93
	s_waitcnt lgkmcnt(2)
	v_add_f32_e32 v3, v3, v94
	ds_bpermute_b32 v94, v34, v102
	ds_bpermute_b32 v91, v37, v3
	s_waitcnt lgkmcnt(3)
	v_add_f32_e32 v3, v92, v101
	s_waitcnt lgkmcnt(2)
	v_add_f32_e32 v92, v93, v99
	ds_bpermute_b32 v93, v32, v92
	s_waitcnt lgkmcnt(2)
	v_add_f32_e32 v94, v102, v94
	ds_bpermute_b32 v99, v33, v94
	v_cvt_f32_i32_e32 v101, v90
	ds_bpermute_b32 v90, v37, v3
	s_waitcnt lgkmcnt(2)
	v_add_f32_e32 v3, v92, v93
	v_cvt_f32_i32_e32 v92, v88
	ds_bpermute_b32 v93, v34, v101
	s_waitcnt lgkmcnt(2)
	v_add_f32_e32 v94, v94, v99
	ds_bpermute_b32 v99, v32, v94
	ds_bpermute_b32 v102, v34, v92
	ds_bpermute_b32 v88, v37, v3
	s_waitcnt lgkmcnt(3)
	v_add_f32_e32 v3, v101, v93
	ds_bpermute_b32 v93, v33, v3
	s_waitcnt lgkmcnt(3)
	v_add_f32_e32 v94, v94, v99
	s_waitcnt lgkmcnt(2)
	v_add_f32_e32 v99, v92, v102
	ds_bpermute_b32 v101, v33, v99
	v_cvt_f32_i32_e32 v87, v87
	s_waitcnt lgkmcnt(1)
	v_add_f32_e32 v3, v3, v93
	ds_bpermute_b32 v92, v37, v94
	ds_bpermute_b32 v93, v32, v3
	s_waitcnt lgkmcnt(2)
	v_add_f32_e32 v94, v99, v101
	ds_bpermute_b32 v101, v34, v87
	ds_bpermute_b32 v99, v32, v94
	v_cvt_f32_i32_e32 v86, v86
	s_waitcnt lgkmcnt(2)
	v_add_f32_e32 v3, v3, v93
	ds_bpermute_b32 v104, v37, v3
	s_waitcnt lgkmcnt(2)
	v_add_f32_e32 v87, v87, v101
	ds_bpermute_b32 v93, v34, v86
	s_waitcnt lgkmcnt(2)
	v_add_f32_e32 v3, v94, v99
	ds_bpermute_b32 v94, v33, v87
	v_cvt_f32_i32_e32 v85, v85
	ds_bpermute_b32 v110, v37, v3
	s_waitcnt lgkmcnt(2)
	v_add_f32_e32 v86, v86, v93
	ds_bpermute_b32 v93, v33, v86
	s_waitcnt lgkmcnt(2)
	v_add_f32_e32 v3, v87, v94
	ds_bpermute_b32 v87, v34, v85
	ds_bpermute_b32 v94, v32, v3
	v_cvt_f32_i32_e32 v84, v84
	s_waitcnt lgkmcnt(2)
	v_add_f32_e32 v86, v86, v93
	ds_bpermute_b32 v93, v32, v86
	s_waitcnt lgkmcnt(2)
	v_add_f32_e32 v85, v85, v87
	ds_bpermute_b32 v87, v33, v85
	s_waitcnt lgkmcnt(2)
	v_add_f32_e32 v3, v3, v94
	ds_bpermute_b32 v94, v34, v84
	ds_bpermute_b32 v112, v37, v3
	s_waitcnt lgkmcnt(3)
	v_add_f32_e32 v3, v86, v93
	s_waitcnt lgkmcnt(2)
	v_add_f32_e32 v85, v85, v87
	ds_bpermute_b32 v86, v32, v85
	s_waitcnt lgkmcnt(2)
	v_add_f32_e32 v84, v84, v94
	v_cvt_f32_i32_e32 v93, v83
	ds_bpermute_b32 v87, v33, v84
	ds_bpermute_b32 v83, v37, v3
	s_waitcnt lgkmcnt(2)
	v_add_f32_e32 v3, v85, v86
	v_cvt_f32_i32_e32 v85, v82
	ds_bpermute_b32 v86, v34, v93
	s_waitcnt lgkmcnt(2)
	v_add_f32_e32 v84, v84, v87
	ds_bpermute_b32 v87, v32, v84
	ds_bpermute_b32 v94, v34, v85
	ds_bpermute_b32 v82, v37, v3
	s_waitcnt lgkmcnt(3)
	v_add_f32_e32 v3, v93, v86
	ds_bpermute_b32 v86, v33, v3
	s_waitcnt lgkmcnt(3)
	v_add_f32_e32 v84, v84, v87
	s_waitcnt lgkmcnt(2)
	v_add_f32_e32 v85, v85, v94
	ds_bpermute_b32 v87, v33, v85
	v_cvt_f32_i32_e32 v81, v81
	s_waitcnt lgkmcnt(1)
	v_add_f32_e32 v3, v3, v86
	ds_bpermute_b32 v86, v32, v3
	v_cvt_f32_i32_e32 v76, v76
	s_waitcnt lgkmcnt(1)
	v_add_f32_e32 v85, v85, v87
	v_cvt_f32_i32_e32 v87, v80
	ds_bpermute_b32 v94, v34, v81
	ds_bpermute_b32 v93, v32, v85
	s_waitcnt lgkmcnt(2)
	v_add_f32_e32 v3, v3, v86
	ds_bpermute_b32 v86, v34, v87
	ds_bpermute_b32 v80, v37, v3
	s_waitcnt lgkmcnt(3)
	v_add_f32_e32 v81, v81, v94
	s_waitcnt lgkmcnt(2)
	v_add_f32_e32 v3, v85, v93
	ds_bpermute_b32 v85, v33, v81
	s_waitcnt lgkmcnt(2)
	v_add_f32_e32 v86, v87, v86
	v_cvt_f32_i32_e32 v87, v79
	ds_bpermute_b32 v93, v33, v86
	ds_bpermute_b32 v79, v37, v3
	s_waitcnt lgkmcnt(2)
	v_add_f32_e32 v3, v81, v85
	ds_bpermute_b32 v81, v34, v87
	ds_bpermute_b32 v85, v32, v3
	v_cvt_f32_i32_e32 v94, v78
	s_waitcnt lgkmcnt(3)
	v_add_f32_e32 v86, v86, v93
	ds_bpermute_b32 v93, v32, v86
	s_waitcnt lgkmcnt(2)
	v_add_f32_e32 v81, v87, v81
	ds_bpermute_b32 v87, v33, v81
	s_waitcnt lgkmcnt(2)
	v_add_f32_e32 v3, v3, v85
	ds_bpermute_b32 v85, v34, v94
	ds_bpermute_b32 v78, v37, v3
	s_waitcnt lgkmcnt(3)
	v_add_f32_e32 v3, v86, v93
	s_waitcnt lgkmcnt(2)
	v_add_f32_e32 v86, v81, v87
	ds_bpermute_b32 v87, v32, v86
	s_waitcnt lgkmcnt(2)
; __device__ __forceinline__ void peer_expert_phase(const Args& a, int layer, LAS unsigned char* lds, int G, int bid) {
;     ...
;         float pa[4], pb[4];
; #pragma unroll
;         for (int i = 0; i < 4; ++i) { pa[i] = 0.f; pb[i] = 0.f;
; #pragma unroll
;             for (int c = 0; c < 16; ++c) { float v = (float)pacc[i][c]; v += __shfl_xor(v, 1); v += __shfl_xor(v, 2); v += __shfl_xor(v, 4);
;                 const float t = __shfl(v, 8 * (lane & 7));
;                 if (c < 8) pa[i] = (g8 == c) ? t : pa[i]; else pb[i] = (g8 == c - 8) ? t : pb[i]; } }
;         float wa[4], wb[4], ssq[4], hgm[4] = {0.f, 0.f, 0.f, 0.f};
; #pragma unroll
;         for (int i = 0; i < 4; ++i) { int tok = tb + i * NGW; tok = tok < NTOK ? tok : tb;
;             const float rstd_t = 1.0f / sqrtf(wave_sum(((const float*)(ws + WS_SSP))[((size_t)layer * NTOK + tok) * 64 + lane]) * (1.0f / DM) + EPS);
	v_add_f32_e32 v85, v94, v85
	ds_bpermute_b32 v93, v33, v85
	v_cvt_f32_i32_e32 v94, v77
	ds_bpermute_b32 v81, v37, v3
	s_waitcnt lgkmcnt(2)
	v_add_f32_e32 v3, v86, v87
	ds_bpermute_b32 v77, v37, v3
	ds_bpermute_b32 v86, v34, v94
	s_waitcnt lgkmcnt(3)
	v_add_f32_e32 v85, v85, v93
	ds_bpermute_b32 v87, v32, v85
	ds_bpermute_b32 v93, v34, v76
	v_cvt_f32_i32_e32 v75, v75
	s_waitcnt lgkmcnt(2)
	v_add_f32_e32 v3, v94, v86
	ds_bpermute_b32 v86, v33, v3
	s_waitcnt lgkmcnt(2)
	v_add_f32_e32 v85, v85, v87
	s_waitcnt lgkmcnt(1)
	v_add_f32_e32 v87, v76, v93
	ds_bpermute_b32 v93, v33, v87
	ds_bpermute_b32 v76, v37, v85
	s_waitcnt lgkmcnt(2)
	v_add_f32_e32 v3, v3, v86
	ds_bpermute_b32 v85, v32, v3
	ds_bpermute_b32 v94, v34, v75
	s_waitcnt lgkmcnt(3)
	v_add_f32_e32 v86, v87, v93
	v_cvt_f32_i32_e32 v87, v74
	ds_bpermute_b32 v93, v32, v86
	s_waitcnt lgkmcnt(2)
	v_add_f32_e32 v3, v3, v85
	s_waitcnt lgkmcnt(1)
	v_add_f32_e32 v75, v75, v94
	ds_bpermute_b32 v85, v34, v87
	ds_bpermute_b32 v74, v37, v3
	s_waitcnt lgkmcnt(2)
	v_add_f32_e32 v3, v86, v93
	ds_bpermute_b32 v86, v33, v75
	v_cvt_f32_i32_e32 v94, v72
	s_waitcnt lgkmcnt(2)
	v_add_f32_e32 v85, v87, v85
	v_cvt_f32_i32_e32 v87, v73
	ds_bpermute_b32 v73, v37, v3
	s_waitcnt lgkmcnt(1)
	v_add_f32_e32 v3, v75, v86
	ds_bpermute_b32 v93, v33, v85
	ds_bpermute_b32 v75, v34, v87
	ds_bpermute_b32 v86, v32, v3
	v_cvt_f32_i32_e32 v69, v69
	v_cvt_f32_i32_e32 v68, v68
	s_waitcnt lgkmcnt(2)
	v_add_f32_e32 v85, v85, v93
	s_waitcnt lgkmcnt(1)
	v_add_f32_e32 v75, v87, v75
	ds_bpermute_b32 v87, v33, v75
	ds_bpermute_b32 v93, v32, v85
	s_waitcnt lgkmcnt(2)
	v_add_f32_e32 v3, v3, v86
	ds_bpermute_b32 v86, v34, v94
	ds_bpermute_b32 v72, v37, v3
	s_waitcnt lgkmcnt(3)
	v_add_f32_e32 v75, v75, v87
	s_waitcnt lgkmcnt(2)
	v_add_f32_e32 v3, v85, v93
	ds_bpermute_b32 v85, v32, v75
	v_cvt_f32_i32_e32 v93, v71
	s_waitcnt lgkmcnt(2)
	v_add_f32_e32 v86, v94, v86
	ds_bpermute_b32 v71, v37, v3
	ds_bpermute_b32 v87, v33, v86
	s_waitcnt lgkmcnt(2)
	v_add_f32_e32 v3, v75, v85
	ds_bpermute_b32 v85, v34, v93
	v_cvt_f32_i32_e32 v75, v70
	ds_bpermute_b32 v70, v37, v3
	s_waitcnt lgkmcnt(2)
	v_add_f32_e32 v86, v86, v87
	ds_bpermute_b32 v87, v32, v86
	s_waitcnt lgkmcnt(2)
	v_add_f32_e32 v3, v93, v85
	ds_bpermute_b32 v85, v33, v3
	ds_bpermute_b32 v94, v34, v75
	s_lshl_b64 s[60:61], s[26:27], 8
	s_waitcnt lgkmcnt(2)
	v_add_f32_e32 v86, v86, v87
	v_cvt_f32_i32_e32 v101, v66
	s_waitcnt lgkmcnt(1)
	v_add_f32_e32 v3, v3, v85
	s_waitcnt lgkmcnt(0)
	v_add_f32_e32 v87, v75, v94
	ds_bpermute_b32 v85, v32, v3
	ds_bpermute_b32 v93, v33, v87
	ds_bpermute_b32 v75, v37, v86
	ds_bpermute_b32 v94, v34, v69
	v_cvt_f32_i32_e32 v64, v64
	s_waitcnt lgkmcnt(3)
	v_add_f32_e32 v3, v3, v85
	s_waitcnt lgkmcnt(2)
	v_add_f32_e32 v87, v87, v93
	ds_bpermute_b32 v86, v37, v3
	ds_bpermute_b32 v3, v34, v68
	ds_bpermute_b32 v93, v32, v87
	s_waitcnt lgkmcnt(3)
	v_add_f32_e32 v69, v69, v94
	v_cvt_f32_i32_e32 v63, v63
	v_cvt_f32_i32_e32 v62, v62
	s_waitcnt lgkmcnt(1)
	v_add_f32_e32 v3, v68, v3
	s_waitcnt lgkmcnt(0)
	v_add_f32_e32 v85, v87, v93
	ds_bpermute_b32 v87, v33, v69
	ds_bpermute_b32 v68, v33, v3
	v_cvt_f32_i32_e32 v93, v67
	ds_bpermute_b32 v67, v37, v85
	v_cvt_f32_i32_e32 v61, v61
	s_waitcnt lgkmcnt(2)
	v_add_f32_e32 v87, v69, v87
	s_waitcnt lgkmcnt(1)
	v_add_f32_e32 v3, v3, v68
	v_lshl_add_u64 v[68:69], v[12:13], 0, s[60:61]
	global_load_dword v102, v[68:69], off
	ds_bpermute_b32 v85, v34, v93
	ds_bpermute_b32 v68, v34, v101
	ds_bpermute_b32 v94, v32, v87
	ds_bpermute_b32 v99, v32, v3
	v_cvt_f32_i32_e32 v60, v60
	s_waitcnt lgkmcnt(3)
	v_add_f32_e32 v85, v93, v85
	ds_bpermute_b32 v93, v33, v85
	s_waitcnt lgkmcnt(3)
	v_add_f32_e32 v68, v101, v68
	s_waitcnt lgkmcnt(2)
	v_add_f32_e32 v66, v87, v94
	ds_bpermute_b32 v87, v33, v68
	s_waitcnt lgkmcnt(2)
	v_add_f32_e32 v3, v3, v99
	s_waitcnt lgkmcnt(1)
	v_add_f32_e32 v69, v85, v93
	ds_bpermute_b32 v85, v32, v69
	v_cvt_f32_i32_e32 v93, v65
	ds_bpermute_b32 v65, v37, v3
	s_waitcnt lgkmcnt(2)
	v_add_f32_e32 v68, v68, v87
	ds_bpermute_b32 v94, v34, v64
	s_waitcnt lgkmcnt(2)
	v_add_f32_e32 v3, v69, v85
	ds_bpermute_b32 v69, v34, v93
	ds_bpermute_b32 v87, v32, v68
	ds_bpermute_b32 v85, v37, v3
	s_waitcnt lgkmcnt(3)
	v_add_f32_e32 v64, v64, v94
	ds_bpermute_b32 v94, v34, v63
	s_waitcnt lgkmcnt(3)
	v_add_f32_e32 v3, v93, v69
	ds_bpermute_b32 v93, v33, v3
	s_waitcnt lgkmcnt(3)
	v_add_f32_e32 v68, v68, v87
	ds_bpermute_b32 v87, v33, v64
	ds_bpermute_b32 v69, v37, v68
	s_waitcnt lgkmcnt(3)
	v_add_f32_e32 v63, v63, v94
	s_waitcnt lgkmcnt(2)
	v_add_f32_e32 v3, v3, v93
	ds_bpermute_b32 v68, v32, v3
	s_waitcnt lgkmcnt(2)
	v_add_f32_e32 v64, v64, v87
	ds_bpermute_b32 v87, v32, v64
	v_cvt_f32_i32_e32 v59, v59
	v_lshl_add_u64 v[120:121], v[14:15], 0, s[22:23]
	s_waitcnt lgkmcnt(1)
	v_add_f32_e32 v3, v3, v68
	ds_bpermute_b32 v68, v34, v62
	ds_bpermute_b32 v93, v37, v3
	s_waitcnt lgkmcnt(2)
	v_add_f32_e32 v3, v64, v87
	ds_bpermute_b32 v64, v33, v63
	ds_bpermute_b32 v99, v37, v3
	s_waitcnt lgkmcnt(3)
; __device__ __forceinline__ float gelu_tanh(float x) { const float u = 0.7978845608028654f * (x + 0.044715f * x * x * x); return 0.5f * x * (1.0f + tanhf(u)); }
; __device__ __forceinline__ void peer_expert_phase(const Args& a, int layer, LAS unsigned char* lds, int G, int bid) {
;     ...
;         float pa[4], pb[4];
; #pragma unroll
;         for (int i = 0; i < 4; ++i) { pa[i] = 0.f; pb[i] = 0.f;
; #pragma unroll
;             for (int c = 0; c < 16; ++c) { float v = (float)pacc[i][c]; v += __shfl_xor(v, 1); v += __shfl_xor(v, 2); v += __shfl_xor(v, 4);
;                 const float t = __shfl(v, 8 * (lane & 7));
;                 if (c < 8) pa[i] = (g8 == c) ? t : pa[i]; else pb[i] = (g8 == c - 8) ? t : pb[i]; } }
;         float wa[4], wb[4], ssq[4], hgm[4] = {0.f, 0.f, 0.f, 0.f};
; #pragma unroll
;         for (int i = 0; i < 4; ++i) { int tok = tb + i * NGW; tok = tok < NTOK ? tok : tb;
;             const float rstd_t = 1.0f / sqrtf(wave_sum(((const float*)(ws + WS_SSP))[((size_t)layer * NTOK + tok) * 64 + lane]) * (1.0f / DM) + EPS);
;             const float ga = GATE[(size_t)tok * 128 + lane], gb = GATE[(size_t)tok * 128 + 64 + lane];
;             const float rx = rstd_t * xs[i];
;             wa[i] = ga * gelu_tanh(pa[i] * SCU[ea[i]] * rx) * SCV[ea[i]]; wb[i] = gb * gelu_tanh(pb[i] * SCU[eb[i]] * rx) * SCV[eb[i]]; ssq[i] = 0.f; }
	v_add_f32_e32 v62, v62, v68
	ds_bpermute_b32 v68, v33, v62
	v_cvt_f32_i32_e32 v23, v23
	s_waitcnt lgkmcnt(2)
	v_add_f32_e32 v3, v63, v64
	ds_bpermute_b32 v63, v34, v61
	ds_bpermute_b32 v64, v32, v3
	s_waitcnt lgkmcnt(2)
	v_add_f32_e32 v62, v62, v68
	ds_bpermute_b32 v68, v32, v62
	v_cvt_f32_i32_e32 v21, v21
	s_waitcnt lgkmcnt(2)
	v_add_f32_e32 v61, v61, v63
	ds_bpermute_b32 v63, v33, v61
	s_waitcnt lgkmcnt(2)
	v_add_f32_e32 v3, v3, v64
	ds_bpermute_b32 v64, v34, v60
	ds_bpermute_b32 v94, v37, v3
	s_waitcnt lgkmcnt(3)
	v_add_f32_e32 v3, v62, v68
	s_waitcnt lgkmcnt(2)
	v_add_f32_e32 v62, v61, v63
	ds_bpermute_b32 v63, v32, v62
	s_waitcnt lgkmcnt(2)
	v_add_f32_e32 v60, v60, v64
	ds_bpermute_b32 v64, v33, v60
	ds_bpermute_b32 v61, v37, v3
	v_cvt_f32_i32_e32 v7, v7
	s_waitcnt lgkmcnt(2)
	v_add_f32_e32 v3, v62, v63
	ds_bpermute_b32 v63, v34, v59
	ds_bpermute_b32 v62, v37, v3
	s_waitcnt lgkmcnt(3)
	v_add_f32_e32 v3, v60, v64
	v_cvt_f32_i32_e32 v64, v19
	v_ashrrev_i32_e32 v19, 31, v18
	s_waitcnt lgkmcnt(1)
	v_add_f32_e32 v63, v59, v63
	v_lshl_add_u64 v[122:123], v[18:19], 2, s[36:37]
	global_load_dword v59, v[120:121], off
	global_load_dword v60, v[120:121], off offset:256
	s_nop 0
	global_load_dword v120, v[122:123], off
	ds_bpermute_b32 v101, v34, v64
	ds_bpermute_b32 v87, v33, v63
	ds_bpermute_b32 v68, v32, v3
	ds_bpermute_b32 v84, v37, v84
	ds_bpermute_b32 v66, v37, v66
	s_waitcnt lgkmcnt(4)
	v_add_f32_e32 v64, v64, v101
	ds_bpermute_b32 v101, v33, v64
	s_waitcnt lgkmcnt(4)
	v_add_f32_e32 v63, v63, v87
	s_waitcnt vmcnt(3)
	ds_bpermute_b32 v113, v29, v102
	ds_bpermute_b32 v87, v32, v63
	s_waitcnt lgkmcnt(5)
	v_add_f32_e32 v3, v3, v68
	s_waitcnt lgkmcnt(2)
	v_add_f32_e32 v64, v64, v101
	ds_bpermute_b32 v68, v37, v3
	s_waitcnt lgkmcnt(2)
	v_add_f32_e32 v101, v102, v113
	ds_bpermute_b32 v102, v30, v101
	s_waitcnt lgkmcnt(2)
	v_add_f32_e32 v3, v63, v87
	ds_bpermute_b32 v63, v34, v23
	ds_bpermute_b32 v87, v37, v3
	ds_bpermute_b32 v113, v32, v64
	s_waitcnt lgkmcnt(3)
	v_add_f32_e32 v3, v101, v102
	ds_bpermute_b32 v101, v31, v3
	s_waitcnt lgkmcnt(3)
	v_add_f32_e32 v23, v23, v63
	ds_bpermute_b32 v63, v33, v23
	s_waitcnt lgkmcnt(2)
	v_add_f32_e32 v64, v64, v113
	s_waitcnt lgkmcnt(1)
	v_add_f32_e32 v3, v3, v101
	ds_bpermute_b32 v102, v32, v3
	s_waitcnt lgkmcnt(1)
	v_add_f32_e32 v23, v23, v63
	ds_bpermute_b32 v63, v32, v23
	ds_bpermute_b32 v101, v37, v64
	ds_bpermute_b32 v64, v34, v21
	s_waitcnt lgkmcnt(3)
	v_add_f32_e32 v3, v3, v102
	s_waitcnt lgkmcnt(2)
	v_add_f32_e32 v23, v23, v63
	ds_bpermute_b32 v63, v33, v3
	s_waitcnt lgkmcnt(1)
	v_add_f32_e32 v21, v21, v64
	ds_bpermute_b32 v64, v33, v21
	ds_bpermute_b32 v102, v37, v23
	ds_bpermute_b32 v23, v34, v7
	s_waitcnt lgkmcnt(3)
	v_add_f32_e32 v3, v3, v63
	ds_bpermute_b32 v63, v34, v3
	s_waitcnt lgkmcnt(3)
	v_add_f32_e32 v21, v21, v64
	ds_bpermute_b32 v64, v32, v21
	s_waitcnt lgkmcnt(2)
	v_add_f32_e32 v7, v7, v23
	ds_bpermute_b32 v23, v33, v7
	s_waitcnt lgkmcnt(2)
	v_add_f32_e32 v3, v3, v63
	v_fmamk_f32 v3, v3, 0x39800000, v47
	v_mul_f32_e32 v63, 0x4f800000, v3
	v_cmp_gt_f32_e32 vcc, s72, v3
	s_waitcnt lgkmcnt(1)
	v_add_f32_e32 v21, v21, v64
	s_waitcnt lgkmcnt(0)
	v_add_f32_e32 v7, v7, v23
	v_cndmask_b32_e32 v3, v3, v63, vcc
	v_sqrt_f32_e32 v63, v3
	ds_bpermute_b32 v23, v32, v7
	v_add_u32_e32 v64, -1, v63
	v_fma_f32 v113, -v64, v63, v3
	v_cmp_ge_f32_e64 s[22:23], 0, v113
	v_add_u32_e32 v113, 1, v63
	s_waitcnt lgkmcnt(0)
	v_add_f32_e32 v7, v7, v23
	v_cndmask_b32_e64 v64, v63, v64, s[22:23]
	v_fma_f32 v63, -v113, v63, v3
	v_cmp_lt_f32_e64 s[22:23], 0, v63
	ds_bpermute_b32 v114, v37, v7
	s_nop 0
	v_cndmask_b32_e64 v63, v64, v113, s[22:23]
	v_mul_f32_e32 v64, 0x37800000, v63
	v_cndmask_b32_e32 v63, v63, v64, vcc
	v_cmp_class_f32_e32 vcc, v3, v48
	ds_bpermute_b32 v113, v37, v21
	s_nop 0
	v_cndmask_b32_e32 v3, v63, v3, vcc
	v_div_scale_f32 v63, s[22:23], v3, v3, 1.0
	v_rcp_f32_e32 v64, v63
	s_nop 0
	v_fma_f32 v7, -v63, v64, 1.0
	v_fmac_f32_e32 v64, v7, v64
	v_div_scale_f32 v7, vcc, 1.0, v3, 1.0
	v_mul_f32_e32 v21, v7, v64
	v_fma_f32 v23, -v63, v21, v7
	v_fmac_f32_e32 v21, v23, v64
	v_fma_f32 v7, -v63, v21, v7
	v_div_fmas_f32 v7, v7, v64, v21
	v_div_fixup_f32 v121, v7, v3, 1.0
	s_waitcnt vmcnt(0)
	v_pk_mul_f32 v[26:27], v[26:27], v[120:121]
	s_nop 0
	v_mul_f32_e32 v26, v26, v27
	v_mul_f32_e32 v3, 0x3d372713, v26
	v_mul_f32_e32 v3, v26, v3
	v_fma_f32 v3, v26, v3, v26
	v_mul_f32_e32 v63, 0x3f4c422a, v3
	v_cmp_nlt_f32_e64 s[22:23], |v63|, s73
	s_and_saveexec_b64 s[60:61], s[22:23]
	s_xor_b64 s[22:23], exec, s[60:61]
	s_cbranch_execz .LBB0_2270
	v_add_f32_e64 v3, |v63|, |v63|
	v_mul_f32_e32 v7, 0x3fb8aa3b, v3
	v_rndne_f32_e32 v21, v7
	v_sub_f32_e32 v23, v7, v21
	v_fma_f32 v7, v3, s74, -v7
	v_fmac_f32_e32 v7, 0x32a5705f, v3
	v_add_f32_e32 v7, v23, v7
	v_cvt_i32_f32_e32 v21, v21
	v_exp_f32_e32 v7, v7
	v_cmp_ngt_f32_e32 vcc, s75, v3
	v_ldexp_f32 v7, v7, v21
	s_nop 0
	v_cndmask_b32_e32 v7, 0, v7, vcc
	v_cmp_nlt_f32_e32 vcc, s76, v3
	s_nop 1
	v_cndmask_b32_e32 v3, v50, v7, vcc
	v_add_f32_e32 v3, 1.0, v3
	v_rcp_f32_e32 v3, v3
	s_nop 0
	v_fma_f32 v64, v3, -2.0, 1.0
